# S1 light-item state-update MFMA blocks + N2 router pass: LDS fragment reads issued two steps ahead (rotating register sets incl. v244-255) instead of just-in-time
# speedup vs baseline: 1.0057x; 1.0017x over previous
.LBB0_303:
	s_add_i32 s52, s52, 1
	v_readlane_b32 s6, v243, 43
	s_mul_i32 s6, s52, s6
	s_mul_hi_u32 s7, s52, s73
	s_add_i32 s7, s7, s6
	s_mul_i32 s6, s52, s73
	s_add_u32 s20, s6, s74
	v_readlane_b32 s6, v242, 23
	s_addc_u32 s21, s7, s6
	v_mov_b64_e32 v[196:197], 0x924
	v_mov_b64_e32 v[198:199], 0x923
	v_cmp_gt_i64_e32 vcc, s[20:21], v[198:199]
	v_cmp_lt_i64_e64 s[6:7], s[20:21], v[196:197]
	s_cbranch_vccnz .LBB0_309
	s_ashr_i32 s16, s20, 31
	s_lshr_b32 s16, s16, 29
	s_add_i32 s18, s20, s16
	s_and_b32 s16, s18, -8
	s_sub_i32 s19, s20, s16
	s_cmp_gt_i32 s19, 3
	s_mov_b64 s[16:17], -1
	s_cbranch_scc0 .LBB0_306
	s_mul_i32 s16, s19, 0x124
	s_add_i32 s20, s16, 4
	s_mov_b64 s[16:17], 0

.LBB0_471:
	s_mul_hi_i32 s21, s20, 0x82082083
	s_add_i32 s21, s21, s20
	s_lshr_b32 s27, s21, 31
	s_ashr_i32 s44, s21, 5
	s_add_i32 s44, s44, s27
	s_mul_i32 s21, s44, 63
	s_sub_i32 s20, s20, s21
	s_add_i32 s27, s20, 1
	s_and_b32 s29, s44, 1
	s_sub_i32 s28, 64, s20
	s_cmp_eq_u32 s29, 0
	s_cselect_b64 s[38:39], -1, 0
	s_and_b64 s[20:21], s[38:39], exec
	s_cselect_b32 s27, s27, s28
	s_bitcmp0_b32 s44, 3
	v_add_u32_e32 v172, s1, v169
	s_mul_i32 s28, s44, 0x41
	s_cbranch_scc1 .LBB0_474
	s_bfe_u32 s20, s44, 0x20001
	s_lshl_b32 s21, s29, 4
	s_lshl_b32 s40, s20, 2
	s_or_b32 s21, s21, s40
	v_readlane_b32 s40, v241, 6
	v_mov_b32_e32 v0, s21
	v_readlane_b32 s41, v241, 7
	s_mov_b32 s21, 0xc2ce8ed0
	s_lshl_b32 s42, s20, 8
	v_readlane_b32 s51, v241, 27
	s_nop 1
	global_load_dword v0, v0, s[40:41]
	s_lshl_b32 s40, s27, 8
	s_waitcnt vmcnt(0)
	v_mul_f32_e32 v1, 0x3fb8aa3b, v0
	v_fma_f32 v2, v0, s94, -v1
	v_rndne_f32_e32 v3, v1
	v_fmac_f32_e32 v2, 0x32a5705f, v0
	v_sub_f32_e32 v1, v1, v3
	v_add_f32_e32 v1, v1, v2
	v_exp_f32_e32 v1, v1
	v_cvt_i32_f32_e32 v2, v3
	v_cmp_ngt_f32_e32 vcc, s21, v0
	s_mov_b32 s21, 0x42b17218
	v_ldexp_f32 v1, v1, v2
	v_cndmask_b32_e32 v1, 0, v1, vcc
	v_cmp_nlt_f32_e32 vcc, s21, v0
	s_lshr_b32 s21, s44, 4
	s_mulk_i32 s21, 0x4100
	s_add_i32 s40, s40, s21
	s_and_b64 s[20:21], s[38:39], exec
	s_cselect_b32 s20, 0, 0xc0
	s_or_b32 s50, s40, s20
	v_cndmask_b32_e32 v9, v204, v1, vcc
	s_and_b64 s[20:21], s[38:39], exec
	v_mul_f32_e32 v0, 0xc2800000, v9
	s_cselect_b32 s41, s88, s58
	v_mul_f32_e32 v0, 0x3fb8aa3b, v0
	s_add_i32 s20, s50, s41
	v_exp_f32_e32 v8, v0
	v_mad_i64_i32 v[0:1], s[20:21], s20, v205, v[140:141]
	s_or_b32 s78, s42, 0x1800
	v_lshl_add_u64 v[2:3], v[0:1], 0, s[78:79]
	global_load_dword v25, v[2:3], off
	s_or_b32 s20, s42, 0x1c00
	s_and_b64 s[42:43], s[38:39], exec
	s_mov_b32 s21, s79
	s_cselect_b32 s42, s61, s63
	v_lshl_add_u64 v[0:1], v[0:1], 0, s[20:21]
	s_add_i32 s43, s50, s42
	global_load_dword v0, v[0:1], off
	v_mad_i64_i32 v[2:3], s[46:47], s43, v205, v[140:141]
	v_lshl_add_u64 v[4:5], v[2:3], 0, s[78:79]
	global_load_dword v29, v[4:5], off
	s_and_b64 s[46:47], s[38:39], exec
	s_cselect_b32 s43, s57, s59
	v_lshl_add_u64 v[2:3], v[2:3], 0, s[20:21]
	s_add_i32 s45, s50, s43
	global_load_dword v1, v[2:3], off
	v_mad_i64_i32 v[2:3], s[46:47], s45, v205, v[140:141]
	v_lshl_add_u64 v[4:5], v[2:3], 0, s[78:79]
	global_load_dword v31, v[4:5], off
	s_and_b64 s[46:47], s[38:39], exec
	s_cselect_b32 s45, s60, s66
	v_lshl_add_u64 v[2:3], v[2:3], 0, s[20:21]
	s_add_i32 s46, s50, s45
	global_load_dword v2, v[2:3], off
	v_mad_i64_i32 v[4:5], s[46:47], s46, v205, v[140:141]
	v_lshl_add_u64 v[6:7], v[4:5], 0, s[78:79]
	global_load_dword v32, v[6:7], off
	s_and_b64 s[46:47], s[38:39], exec
	s_cselect_b32 s46, s85, s89
	v_lshl_add_u64 v[4:5], v[4:5], 0, s[20:21]
	s_add_i32 s47, s50, s46
	global_load_dword v3, v[4:5], off
	v_mad_i64_i32 v[4:5], s[48:49], s47, v205, v[140:141]
	v_lshl_add_u64 v[6:7], v[4:5], 0, s[78:79]
	s_and_b64 s[48:49], s[38:39], exec
	v_readlane_b32 s47, v241, 45
	global_load_dword v33, v[6:7], off
	s_cselect_b32 s47, s97, s47
	v_lshl_add_u64 v[4:5], v[4:5], 0, s[20:21]
	s_add_i32 s48, s50, s47
	global_load_dword v27, v[4:5], off
	v_mad_i64_i32 v[4:5], s[48:49], s48, v205, v[140:141]
	s_and_b64 s[48:49], s[38:39], exec
	v_readlane_b32 s48, v241, 19
	v_readlane_b32 s49, v241, 23
	s_cselect_b32 s48, s48, s49
	v_lshl_add_u64 v[6:7], v[4:5], 0, s[78:79]
	v_lshl_add_u64 v[4:5], v[4:5], 0, s[20:21]
	s_add_i32 s49, s50, s48
	global_load_dword v34, v[6:7], off
	global_load_dword v28, v[4:5], off
	v_mad_i64_i32 v[4:5], s[52:53], s49, v205, v[140:141]
	s_and_b64 s[52:53], s[38:39], exec
	v_readlane_b32 s49, v241, 21
	s_cselect_b32 s49, s49, s51
	v_lshl_add_u64 v[6:7], v[4:5], 0, s[78:79]
	v_lshl_add_u64 v[4:5], v[4:5], 0, s[20:21]
	s_add_i32 s50, s50, s49
	global_load_dword v35, v[6:7], off
	global_load_dword v30, v[4:5], off
	v_mad_i64_i32 v[4:5], s[50:51], s50, v205, v[140:141]
	s_lshl_b32 s52, s29, 6
	s_or_b32 s50, s52, s40
	s_add_i32 s53, s50, 64
	v_lshl_add_u64 v[6:7], v[4:5], 0, s[78:79]
	v_lshl_add_u64 v[4:5], v[4:5], 0, s[20:21]
	s_add_i32 s50, s53, s41
	global_load_dword v37, v[6:7], off
	global_load_dword v36, v[4:5], off
	v_mad_i64_i32 v[4:5], s[50:51], s50, v205, v[140:141]
	v_lshl_add_u64 v[6:7], v[4:5], 0, s[78:79]
	v_lshl_add_u64 v[4:5], v[4:5], 0, s[20:21]
	s_add_i32 s50, s53, s42
	global_load_dword v15, v[6:7], off
	global_load_dword v10, v[4:5], off
	v_mad_i64_i32 v[4:5], s[50:51], s50, v205, v[140:141]
	v_lshl_add_u64 v[6:7], v[4:5], 0, s[78:79]
	v_lshl_add_u64 v[4:5], v[4:5], 0, s[20:21]
	s_add_i32 s50, s53, s43
	global_load_dword v17, v[6:7], off
	global_load_dword v11, v[4:5], off
	v_mad_i64_i32 v[4:5], s[50:51], s50, v205, v[140:141]
	v_lshl_add_u64 v[6:7], v[4:5], 0, s[78:79]
	v_lshl_add_u64 v[4:5], v[4:5], 0, s[20:21]
	s_add_i32 s50, s53, s45
	global_load_dword v19, v[6:7], off
	global_load_dword v12, v[4:5], off
	v_mad_i64_i32 v[4:5], s[50:51], s50, v205, v[140:141]
	v_lshl_add_u64 v[6:7], v[4:5], 0, s[78:79]
	v_lshl_add_u64 v[4:5], v[4:5], 0, s[20:21]
	s_add_i32 s50, s53, s46
	global_load_dword v20, v[6:7], off
	global_load_dword v13, v[4:5], off
	v_mad_i64_i32 v[4:5], s[50:51], s50, v205, v[140:141]
	v_lshl_add_u64 v[6:7], v[4:5], 0, s[78:79]
	v_lshl_add_u64 v[4:5], v[4:5], 0, s[20:21]
	s_add_i32 s50, s53, s47
	global_load_dword v22, v[6:7], off
	global_load_dword v14, v[4:5], off
	v_mad_i64_i32 v[4:5], s[50:51], s50, v205, v[140:141]
	v_lshl_add_u64 v[6:7], v[4:5], 0, s[78:79]
	v_lshl_add_u64 v[4:5], v[4:5], 0, s[20:21]
	s_add_i32 s50, s53, s48
	global_load_dword v23, v[6:7], off
	global_load_dword v16, v[4:5], off
	v_mad_i64_i32 v[4:5], s[50:51], s50, v205, v[140:141]
	v_lshl_add_u64 v[6:7], v[4:5], 0, s[78:79]
	v_lshl_add_u64 v[4:5], v[4:5], 0, s[20:21]
	s_add_i32 s53, s53, s49
	global_load_dword v24, v[6:7], off
	global_load_dword v18, v[4:5], off
	v_mad_i64_i32 v[4:5], s[50:51], s53, v205, v[140:141]
	s_sub_i32 s50, s40, s52
	s_add_i32 s52, s50, 0x80
	v_lshl_add_u64 v[6:7], v[4:5], 0, s[78:79]
	v_lshl_add_u64 v[4:5], v[4:5], 0, s[20:21]
	s_add_i32 s50, s52, s41
	global_load_dword v26, v[6:7], off
	global_load_dword v21, v[4:5], off
	v_mad_i64_i32 v[4:5], s[50:51], s50, v205, v[140:141]
	v_lshl_add_u64 v[6:7], v[4:5], 0, s[78:79]
	v_lshl_add_u64 v[4:5], v[4:5], 0, s[20:21]
	s_add_i32 s50, s52, s42
	global_load_dword v41, v[6:7], off
	s_nop 0
	global_load_dword v4, v[4:5], off
	v_mad_i64_i32 v[6:7], s[50:51], s50, v205, v[140:141]
	v_lshl_add_u64 v[38:39], v[6:7], 0, s[78:79]
	v_lshl_add_u64 v[6:7], v[6:7], 0, s[20:21]
	s_add_i32 s50, s52, s43
	global_load_dword v45, v[38:39], off
	global_load_dword v5, v[6:7], off
	v_mad_i64_i32 v[6:7], s[50:51], s50, v205, v[140:141]
	v_lshl_add_u64 v[38:39], v[6:7], 0, s[78:79]
	v_lshl_add_u64 v[6:7], v[6:7], 0, s[20:21]
	s_add_i32 s50, s52, s45
	global_load_dword v68, v[38:39], off
	s_nop 0
	global_load_dword v6, v[6:7], off
	v_mad_i64_i32 v[38:39], s[50:51], s50, v205, v[140:141]
	v_lshl_add_u64 v[42:43], v[38:39], 0, s[78:79]
	v_lshl_add_u64 v[38:39], v[38:39], 0, s[20:21]
	s_add_i32 s50, s52, s46
	global_load_dword v69, v[42:43], off
	global_load_dword v7, v[38:39], off
	v_mad_i64_i32 v[38:39], s[50:51], s50, v205, v[140:141]
	v_lshl_add_u64 v[42:43], v[38:39], 0, s[78:79]
	v_lshl_add_u64 v[38:39], v[38:39], 0, s[20:21]
	s_add_i32 s50, s52, s47
	global_load_dword v75, v[42:43], off
	global_load_dword v40, v[38:39], off
	v_mad_i64_i32 v[38:39], s[50:51], s50, v205, v[140:141]
	v_lshl_add_u64 v[42:43], v[38:39], 0, s[78:79]
	v_lshl_add_u64 v[38:39], v[38:39], 0, s[20:21]
	s_add_i32 s50, s52, s48
	global_load_dword v77, v[42:43], off
	global_load_dword v44, v[38:39], off
	v_mad_i64_i32 v[38:39], s[50:51], s50, v205, v[140:141]
	v_lshl_add_u64 v[42:43], v[38:39], 0, s[78:79]
	v_lshl_add_u64 v[38:39], v[38:39], 0, s[20:21]
	s_add_i32 s52, s52, s49
	global_load_dword v78, v[42:43], off
	global_load_dword v67, v[38:39], off
	v_mad_i64_i32 v[38:39], s[50:51], s52, v205, v[140:141]
	v_lshl_add_u64 v[42:43], v[38:39], 0, s[78:79]
	v_lshl_add_u64 v[38:39], v[38:39], 0, s[20:21]
	global_load_dword v79, v[42:43], off
	global_load_dword v74, v[38:39], off
	v_mul_f32_e64 v38, v123, -v9
	v_mul_f32_e32 v38, 0x3fb8aa3b, v38
	v_exp_f32_e32 v46, v38
	s_waitcnt vmcnt(47)
	v_lshlrev_b32_e32 v38, 16, v25
	v_and_b32_e32 v25, 0xffff0000, v25
	s_waitcnt lgkmcnt(0)
	v_mul_f32_e32 v38, v46, v38
	v_mul_f32_e32 v25, v46, v25
	s_barrier
	v_cvt_pk_bf16_f32 v25, v38, v25
	v_mul_f32_e64 v38, v162, -v9
	v_mul_f32_e32 v38, 0x3fb8aa3b, v38
	v_exp_f32_e32 v47, v38
	s_waitcnt vmcnt(45)
	v_lshlrev_b32_e32 v38, 16, v29
	v_and_b32_e32 v29, 0xffff0000, v29
	s_and_b64 s[50:51], s[38:39], exec
	v_mul_f32_e32 v38, v47, v38
	v_mul_f32_e32 v29, v47, v29
	v_cvt_pk_bf16_f32 v29, v38, v29
	v_mul_f32_e64 v38, v163, -v9
	v_mul_f32_e32 v38, 0x3fb8aa3b, v38
	v_exp_f32_e32 v48, v38
	s_waitcnt vmcnt(43)
	v_lshlrev_b32_e32 v38, 16, v31
	v_and_b32_e32 v31, 0xffff0000, v31
	s_cselect_b32 s50, 0xc0, 0
	v_mul_f32_e32 v38, v48, v38
	v_mul_f32_e32 v31, v48, v31
	v_cvt_pk_bf16_f32 v31, v38, v31
	v_mul_f32_e64 v38, v164, -v9
	v_mul_f32_e32 v38, 0x3fb8aa3b, v38
	v_exp_f32_e32 v49, v38
	s_waitcnt vmcnt(41)
	v_lshlrev_b32_e32 v38, 16, v32
	v_and_b32_e32 v32, 0xffff0000, v32
	s_or_b32 s50, s40, s50
	v_mul_f32_e32 v38, v49, v38
	v_mul_f32_e32 v32, v49, v32
	v_cvt_pk_bf16_f32 v38, v38, v32
	v_mul_f32_e64 v32, v165, -v9
	v_mul_f32_e32 v32, 0x3fb8aa3b, v32
	v_exp_f32_e32 v50, v32
	s_waitcnt vmcnt(39)
	v_lshlrev_b32_e32 v32, 16, v33
	v_and_b32_e32 v33, 0xffff0000, v33
	s_add_i32 s40, s50, s41
	v_mul_f32_e32 v32, v50, v32
	v_mul_f32_e32 v33, v50, v33
	v_cvt_pk_bf16_f32 v39, v32, v33
	v_mul_f32_e64 v32, v166, -v9
	v_mul_f32_e32 v32, 0x3fb8aa3b, v32
	v_exp_f32_e32 v51, v32
	s_waitcnt vmcnt(37)
	v_lshlrev_b32_e32 v32, 16, v34
	v_and_b32_e32 v33, 0xffff0000, v34
	v_and_b32_e32 v34, 0xffff, v39
	v_mul_f32_e32 v32, v51, v32
	v_mul_f32_e32 v33, v51, v33
	v_cvt_pk_bf16_f32 v42, v32, v33
	v_mul_f32_e64 v32, v167, -v9
	v_mul_f32_e32 v32, 0x3fb8aa3b, v32
	v_exp_f32_e32 v52, v32
	s_waitcnt vmcnt(35)
	v_lshlrev_b32_e32 v32, 16, v35
	v_and_b32_e32 v33, 0xffff0000, v35
	v_lshl_or_b32 v34, v42, 16, v34
	v_mul_f32_e32 v32, v52, v32
	v_mul_f32_e32 v33, v52, v33
	v_cvt_pk_bf16_f32 v43, v32, v33
	v_mul_f32_e64 v32, v168, -v9
	v_mul_f32_e32 v32, 0x3fb8aa3b, v32
	v_exp_f32_e32 v53, v32
	s_waitcnt vmcnt(33)
	v_lshlrev_b32_e32 v32, 16, v37
	v_and_b32_e32 v33, 0xffff0000, v37
	v_and_b32_e32 v35, 0xffff, v43
	v_mul_f32_e32 v32, v53, v32
	v_mul_f32_e32 v33, v53, v33
	v_cvt_pk_bf16_f32 v37, v32, v33
	v_and_b32_e32 v32, 0xffff, v25
	v_lshrrev_b32_e32 v25, 16, v25
	v_and_or_b32 v54, v29, s95, v25
	v_lshrrev_b32_e32 v25, 16, v31
	v_and_or_b32 v55, v38, s95, v25
	v_lshrrev_b32_e32 v25, 16, v39
	v_and_b32_e32 v33, 0xffff, v31
	v_and_or_b32 v56, v42, s95, v25
	v_lshrrev_b32_e32 v25, 16, v43
	v_lshl_or_b32 v32, v29, 16, v32
	v_lshl_or_b32 v33, v38, 16, v33
	v_lshl_or_b32 v35, v37, 16, v35
	v_and_or_b32 v57, v37, s95, v25
	v_and_b32_e32 v25, 0xffff, v0
	ds_write_b128 v171, v[32:35] offset:32768
	ds_write_b128 v171, v[54:57] offset:32832
	v_lshl_or_b32 v32, v1, 16, v25
	v_and_b32_e32 v25, 0xffff, v2
	v_lshl_or_b32 v33, v3, 16, v25
	v_and_b32_e32 v25, 0xffff, v27
	v_lshrrev_b32_e32 v0, 16, v0
	v_lshl_or_b32 v34, v28, 16, v25
	v_and_b32_e32 v25, 0xffff, v30
	v_and_or_b32 v0, v1, s95, v0
	v_lshrrev_b32_e32 v1, 16, v2
	s_waitcnt vmcnt(32)
	v_lshl_or_b32 v35, v36, 16, v25
	v_and_or_b32 v1, v3, s95, v1
	v_lshrrev_b32_e32 v2, 16, v27
	v_lshrrev_b32_e32 v3, 16, v30
	v_and_or_b32 v2, v28, s95, v2
	v_and_or_b32 v3, v36, s95, v3
	ds_write_b128 v171, v[32:35] offset:49152
	ds_write_b128 v171, v[0:3] offset:49216
	v_mad_i64_i32 v[0:1], s[40:41], s40, v205, v[140:141]
	v_lshl_add_u64 v[2:3], v[0:1], 0, s[78:79]
	v_lshl_add_u64 v[0:1], v[0:1], 0, s[20:21]
	s_add_i32 s40, s50, s42
	global_load_dword v59, v[2:3], off
	global_load_dword v54, v[0:1], off
	v_mad_i64_i32 v[0:1], s[40:41], s40, v205, v[140:141]
	v_lshl_add_u64 v[2:3], v[0:1], 0, s[78:79]
	v_lshl_add_u64 v[0:1], v[0:1], 0, s[20:21]
	s_add_i32 s40, s50, s43
	global_load_dword v61, v[2:3], off
	global_load_dword v55, v[0:1], off
	v_mad_i64_i32 v[0:1], s[40:41], s40, v205, v[140:141]
	v_lshl_add_u64 v[2:3], v[0:1], 0, s[78:79]
	v_lshl_add_u64 v[0:1], v[0:1], 0, s[20:21]
	s_add_i32 s40, s50, s45
	global_load_dword v63, v[2:3], off
	global_load_dword v56, v[0:1], off
	v_mad_i64_i32 v[0:1], s[40:41], s40, v205, v[140:141]
	v_lshl_add_u64 v[2:3], v[0:1], 0, s[78:79]
	v_lshl_add_u64 v[0:1], v[0:1], 0, s[20:21]
	s_add_i32 s40, s50, s46
	global_load_dword v66, v[2:3], off
	global_load_dword v57, v[0:1], off
	v_mad_i64_i32 v[0:1], s[40:41], s40, v205, v[140:141]
	v_lshl_add_u64 v[2:3], v[0:1], 0, s[78:79]
	v_lshl_add_u64 v[0:1], v[0:1], 0, s[20:21]
	s_add_i32 s40, s50, s47
	global_load_dword v71, v[2:3], off
	global_load_dword v58, v[0:1], off
	v_mad_i64_i32 v[0:1], s[40:41], s40, v205, v[140:141]
	v_lshl_add_u64 v[2:3], v[0:1], 0, s[78:79]
	v_lshl_add_u64 v[0:1], v[0:1], 0, s[20:21]
	s_add_i32 s40, s50, s48
	global_load_dword v72, v[2:3], off
	global_load_dword v60, v[0:1], off
	v_mad_i64_i32 v[0:1], s[40:41], s40, v205, v[140:141]
	v_lshl_add_u64 v[2:3], v[0:1], 0, s[78:79]
	v_lshl_add_u64 v[0:1], v[0:1], 0, s[20:21]
	s_add_i32 s50, s50, s49
	global_load_dword v73, v[2:3], off
	global_load_dword v62, v[0:1], off
	v_mad_i64_i32 v[0:1], s[40:41], s50, v205, v[140:141]
	v_lshl_add_u64 v[2:3], v[0:1], 0, s[78:79]
	v_lshl_add_u64 v[0:1], v[0:1], 0, s[20:21]
	global_load_dword v76, v[2:3], off
	global_load_dword v70, v[0:1], off
	s_waitcnt lgkmcnt(0)
	s_barrier
	ds_read_b128 v[0:3], v172 offset:32768
	ds_read_b128 v[28:31], v172 offset:33792
	ds_read_b128 v[244:247], v170 offset:49152
	ds_read_b128 v[248:251], v170 offset:50176
	ds_read_b128 v[252:255], v170 offset:51200
	ds_read_b128 v[196:199], v170 offset:52224
	s_waitcnt lgkmcnt(3)
	v_mfma_f32_16x16x32_bf16 v[32:35], v[0:3], v[244:247], 0
	s_waitcnt vmcnt(47)
	v_lshlrev_b32_e32 v25, 16, v15
	v_and_b32_e32 v15, 0xffff0000, v15
	v_mul_f32_e32 v25, v46, v25
	s_waitcnt lgkmcnt(2)
	v_mfma_f32_16x16x32_bf16 v[32:35], v[28:31], v[248:251], v[32:35]
	ds_read_b128 v[244:247], v170 offset:53248
	ds_read_b128 v[248:251], v170 offset:54272
	v_mul_f32_e32 v15, v46, v15
	s_add_i32 s20, s27, s28
	s_ashr_i32 s21, s20, 31
	s_lshl_b64 s[40:41], s[20:21], 15
	v_readlane_b32 s42, v242, 58
	s_nop 2
	v_pk_fma_f32 v[42:43], v[8:9], 0, v[32:33] op_sel_hi:[0,0,1]
	v_pk_fma_f32 v[88:89], v[8:9], 0, v[34:35] op_sel_hi:[0,0,1]
	s_waitcnt lgkmcnt(3)
	v_mfma_f32_16x16x32_bf16 v[32:35], v[0:3], v[252:255], 0
	s_add_u32 s40, s42, s40
	v_readlane_b32 s42, v242, 60
	s_addc_u32 s41, s42, s41
	s_waitcnt lgkmcnt(2)
	v_mfma_f32_16x16x32_bf16 v[32:35], v[28:31], v[196:199], v[32:35]
	ds_read_b128 v[252:255], v170 offset:55296
	ds_read_b128 v[196:199], v170 offset:56320
	s_mov_b64 s[42:43], 0
	s_and_b64 vcc, exec, s[34:35]
	s_nop 5
	v_pk_fma_f32 v[90:91], v[8:9], 0, v[32:33] op_sel_hi:[0,0,1]
	v_pk_fma_f32 v[92:93], v[8:9], 0, v[34:35] op_sel_hi:[0,0,1]
	s_waitcnt lgkmcnt(3)
	v_mfma_f32_16x16x32_bf16 v[32:35], v[0:3], v[244:247], 0
	s_waitcnt lgkmcnt(2)
	v_mfma_f32_16x16x32_bf16 v[32:35], v[28:31], v[248:251], v[32:35]
	ds_read_b128 v[244:247], v170 offset:57344
	ds_read_b128 v[248:251], v170 offset:58368
	s_nop 7
	v_pk_fma_f32 v[94:95], v[8:9], 0, v[32:33] op_sel_hi:[0,0,1]
	v_pk_fma_f32 v[96:97], v[8:9], 0, v[34:35] op_sel_hi:[0,0,1]
	s_waitcnt lgkmcnt(3)
	v_mfma_f32_16x16x32_bf16 v[32:35], v[0:3], v[252:255], 0
	s_waitcnt lgkmcnt(2)
	v_mfma_f32_16x16x32_bf16 v[32:35], v[28:31], v[196:199], v[32:35]
	ds_read_b128 v[252:255], v170 offset:59392
	ds_read_b128 v[196:199], v170 offset:60416
	s_nop 7
	v_pk_fma_f32 v[98:99], v[8:9], 0, v[32:33] op_sel_hi:[0,0,1]
	v_pk_fma_f32 v[100:101], v[8:9], 0, v[34:35] op_sel_hi:[0,0,1]
	s_waitcnt lgkmcnt(3)
	v_mfma_f32_16x16x32_bf16 v[32:35], v[0:3], v[244:247], 0
	s_waitcnt lgkmcnt(2)
	v_mfma_f32_16x16x32_bf16 v[32:35], v[28:31], v[248:251], v[32:35]
	ds_read_b128 v[244:247], v170 offset:61440
	ds_read_b128 v[248:251], v170 offset:62464
	s_nop 7
	v_pk_fma_f32 v[102:103], v[8:9], 0, v[32:33] op_sel_hi:[0,0,1]
	v_pk_fma_f32 v[104:105], v[8:9], 0, v[34:35] op_sel_hi:[0,0,1]
	s_waitcnt lgkmcnt(3)
	v_mfma_f32_16x16x32_bf16 v[32:35], v[0:3], v[252:255], 0
	s_waitcnt lgkmcnt(2)
	v_mfma_f32_16x16x32_bf16 v[32:35], v[28:31], v[196:199], v[32:35]
	ds_read_b128 v[252:255], v170 offset:63488
	ds_read_b128 v[196:199], v170 offset:64512
	s_nop 7
	v_pk_fma_f32 v[106:107], v[8:9], 0, v[32:33] op_sel_hi:[0,0,1]
	v_pk_fma_f32 v[108:109], v[8:9], 0, v[34:35] op_sel_hi:[0,0,1]
	s_waitcnt lgkmcnt(3)
	v_mfma_f32_16x16x32_bf16 v[32:35], v[0:3], v[244:247], 0
	s_waitcnt lgkmcnt(2)
	v_mfma_f32_16x16x32_bf16 v[32:35], v[28:31], v[248:251], v[32:35]
	s_nop 7
	v_pk_fma_f32 v[110:111], v[8:9], 0, v[32:33] op_sel_hi:[0,0,1]
	v_pk_fma_f32 v[112:113], v[8:9], 0, v[34:35] op_sel_hi:[0,0,1]
	v_cvt_pk_bf16_f32 v15, v25, v15
	s_waitcnt vmcnt(45)
	v_lshlrev_b32_e32 v25, 16, v17
	v_and_b32_e32 v17, 0xffff0000, v17
	v_mul_f32_e32 v25, v47, v25
	v_mul_f32_e32 v17, v47, v17
	v_cvt_pk_bf16_f32 v17, v25, v17
	s_waitcnt vmcnt(43)
	v_lshlrev_b32_e32 v25, 16, v19
	v_and_b32_e32 v19, 0xffff0000, v19
	v_mul_f32_e32 v25, v48, v25
	v_mul_f32_e32 v19, v48, v19
	s_waitcnt lgkmcnt(1)
	v_mfma_f32_16x16x32_bf16 v[0:3], v[0:3], v[252:255], 0
	v_cvt_pk_bf16_f32 v19, v25, v19
	s_waitcnt vmcnt(41)
	v_lshlrev_b32_e32 v25, 16, v20
	v_and_b32_e32 v20, 0xffff0000, v20
	v_mul_f32_e32 v25, v49, v25
	v_mul_f32_e32 v20, v49, v20
	v_cvt_pk_bf16_f32 v20, v25, v20
	s_waitcnt vmcnt(39)
	v_lshlrev_b32_e32 v25, 16, v22
	v_and_b32_e32 v22, 0xffff0000, v22
	v_mul_f32_e32 v22, v50, v22
	s_waitcnt lgkmcnt(0)
	v_mfma_f32_16x16x32_bf16 v[0:3], v[28:31], v[196:199], v[0:3]
	v_mul_f32_e32 v25, v50, v25
	v_cvt_pk_bf16_f32 v28, v25, v22
	s_waitcnt vmcnt(37)
	v_lshlrev_b32_e32 v22, 16, v23
	v_mul_f32_e32 v22, v51, v22
	v_and_b32_e32 v23, 0xffff0000, v23
	v_mul_f32_e32 v23, v51, v23
	v_cvt_pk_bf16_f32 v29, v22, v23
	s_waitcnt vmcnt(35)
	v_lshlrev_b32_e32 v22, 16, v24
	v_mul_f32_e32 v22, v52, v22
	v_and_b32_e32 v23, 0xffff0000, v24
	v_mul_f32_e32 v23, v52, v23
	v_cvt_pk_bf16_f32 v30, v22, v23
	s_waitcnt vmcnt(33)
	v_lshlrev_b32_e32 v22, 16, v26
	v_mul_f32_e32 v22, v53, v22
	v_and_b32_e32 v23, 0xffff0000, v26
	v_mul_f32_e32 v23, v53, v23
	v_cvt_pk_bf16_f32 v31, v22, v23
	v_and_b32_e32 v22, 0xffff, v15
	v_lshrrev_b32_e32 v15, 16, v15
	v_and_or_b32 v26, v17, s95, v15
	v_lshrrev_b32_e32 v15, 16, v19
	v_and_or_b32 v27, v20, s95, v15
	v_lshrrev_b32_e32 v15, 16, v28
	v_and_b32_e32 v23, 0xffff, v19
	v_and_b32_e32 v24, 0xffff, v28
	v_and_b32_e32 v25, 0xffff, v30
	v_and_or_b32 v28, v29, s95, v15
	v_lshrrev_b32_e32 v15, 16, v30
	v_lshl_or_b32 v22, v17, 16, v22
	v_lshl_or_b32 v23, v20, 16, v23
	v_lshl_or_b32 v24, v29, 16, v24
	v_lshl_or_b32 v25, v31, 16, v25
	v_and_or_b32 v29, v31, s95, v15
	v_and_b32_e32 v15, 0xffff, v10
	ds_write_b128 v171, v[22:25]
	ds_write_b128 v171, v[26:29] offset:64
	v_lshl_or_b32 v22, v11, 16, v15
	v_and_b32_e32 v15, 0xffff, v12
	v_lshl_or_b32 v23, v13, 16, v15
	v_and_b32_e32 v15, 0xffff, v14
	v_lshrrev_b32_e32 v10, 16, v10
	v_lshl_or_b32 v24, v16, 16, v15
	v_and_b32_e32 v15, 0xffff, v18
	v_and_or_b32 v10, v11, s95, v10
	v_lshrrev_b32_e32 v11, 16, v12
	s_waitcnt vmcnt(32)
	v_lshl_or_b32 v25, v21, 16, v15
	v_and_or_b32 v11, v13, s95, v11
	v_lshrrev_b32_e32 v12, 16, v14
	v_lshrrev_b32_e32 v13, 16, v18
	v_and_or_b32 v12, v16, s95, v12
	v_and_or_b32 v13, v21, s95, v13
	ds_write_b128 v171, v[22:25] offset:16384
	ds_write_b128 v171, v[10:13] offset:16448
	s_waitcnt lgkmcnt(0)
	s_barrier
	ds_read_b128 v[80:83], v172
	ds_read_b128 v[84:87], v172 offset:1024
	ds_read_b128 v[244:247], v170 offset:16384
	ds_read_b128 v[248:251], v170 offset:17408
	ds_read_b128 v[252:255], v170 offset:18432
	ds_read_b128 v[196:199], v170 offset:19456
	s_waitcnt lgkmcnt(3)
	v_mfma_f32_16x16x32_bf16 v[10:13], v[80:83], v[244:247], 0
	v_fma_f32 v0, v8, 0, v0
	v_fma_f32 v1, v8, 0, v1
	v_pk_fma_f32 v[2:3], v[8:9], 0, v[2:3] op_sel_hi:[0,0,1]
	s_waitcnt lgkmcnt(2)
	v_mfma_f32_16x16x32_bf16 v[10:13], v[84:87], v[248:251], v[10:13]
	ds_read_b128 v[244:247], v170 offset:20480
	ds_read_b128 v[248:251], v170 offset:21504
	s_nop 7
	v_pk_fma_f32 v[26:27], v[8:9], v[88:89], v[12:13] op_sel_hi:[0,1,1]
	v_pk_fma_f32 v[14:15], v[8:9], v[42:43], v[10:11] op_sel_hi:[0,1,1]
	s_waitcnt lgkmcnt(3)
	v_mfma_f32_16x16x32_bf16 v[10:13], v[80:83], v[252:255], 0
	s_waitcnt lgkmcnt(2)
	v_mfma_f32_16x16x32_bf16 v[10:13], v[84:87], v[196:199], v[10:13]
	ds_read_b128 v[252:255], v170 offset:22528
	ds_read_b128 v[196:199], v170 offset:23552
	s_nop 7
	v_pk_fma_f32 v[28:29], v[8:9], v[92:93], v[12:13] op_sel_hi:[0,1,1]
	v_pk_fma_f32 v[16:17], v[8:9], v[90:91], v[10:11] op_sel_hi:[0,1,1]
	s_waitcnt lgkmcnt(3)
	v_mfma_f32_16x16x32_bf16 v[10:13], v[80:83], v[244:247], 0
	s_waitcnt lgkmcnt(2)
	v_mfma_f32_16x16x32_bf16 v[10:13], v[84:87], v[248:251], v[10:13]
	ds_read_b128 v[244:247], v170 offset:24576
	ds_read_b128 v[248:251], v170 offset:25600
	s_nop 7
	v_pk_fma_f32 v[30:31], v[8:9], v[96:97], v[12:13] op_sel_hi:[0,1,1]
	v_pk_fma_f32 v[18:19], v[8:9], v[94:95], v[10:11] op_sel_hi:[0,1,1]
	s_waitcnt lgkmcnt(3)
	v_mfma_f32_16x16x32_bf16 v[10:13], v[80:83], v[252:255], 0
	s_waitcnt lgkmcnt(2)
	v_mfma_f32_16x16x32_bf16 v[10:13], v[84:87], v[196:199], v[10:13]
	ds_read_b128 v[252:255], v170 offset:26624
	ds_read_b128 v[196:199], v170 offset:27648
	s_nop 7
	v_pk_fma_f32 v[32:33], v[8:9], v[100:101], v[12:13] op_sel_hi:[0,1,1]
	v_pk_fma_f32 v[20:21], v[8:9], v[98:99], v[10:11] op_sel_hi:[0,1,1]
	s_waitcnt lgkmcnt(3)
	v_mfma_f32_16x16x32_bf16 v[10:13], v[80:83], v[244:247], 0
	s_waitcnt lgkmcnt(2)
	v_mfma_f32_16x16x32_bf16 v[10:13], v[84:87], v[248:251], v[10:13]
	ds_read_b128 v[244:247], v170 offset:28672
	ds_read_b128 v[248:251], v170 offset:29696
	s_nop 7
	v_pk_fma_f32 v[34:35], v[8:9], v[104:105], v[12:13] op_sel_hi:[0,1,1]
	v_pk_fma_f32 v[22:23], v[8:9], v[102:103], v[10:11] op_sel_hi:[0,1,1]
	s_waitcnt lgkmcnt(3)
	v_mfma_f32_16x16x32_bf16 v[10:13], v[80:83], v[252:255], 0
	s_waitcnt lgkmcnt(2)
	v_mfma_f32_16x16x32_bf16 v[10:13], v[84:87], v[196:199], v[10:13]
	ds_read_b128 v[252:255], v170 offset:30720
	ds_read_b128 v[196:199], v170 offset:31744
	s_nop 7
	v_pk_fma_f32 v[36:37], v[8:9], v[108:109], v[12:13] op_sel_hi:[0,1,1]
	v_pk_fma_f32 v[24:25], v[8:9], v[106:107], v[10:11] op_sel_hi:[0,1,1]
	s_waitcnt lgkmcnt(3)
	v_mfma_f32_16x16x32_bf16 v[10:13], v[80:83], v[244:247], 0
	s_waitcnt lgkmcnt(2)
	v_mfma_f32_16x16x32_bf16 v[88:91], v[84:87], v[248:251], v[10:13]
	s_nop 7
	v_pk_fma_f32 v[10:11], v[8:9], v[112:113], v[90:91] op_sel_hi:[0,1,1]
	v_pk_fma_f32 v[12:13], v[8:9], v[110:111], v[88:89] op_sel_hi:[0,1,1]
	s_waitcnt lgkmcnt(1)
	v_mfma_f32_16x16x32_bf16 v[80:83], v[80:83], v[252:255], 0
	s_waitcnt lgkmcnt(0)
	v_mfma_f32_16x16x32_bf16 v[80:83], v[84:87], v[196:199], v[80:83]
	s_nop 7
	v_pk_fma_f32 v[42:43], v[8:9], v[0:1], v[80:81] op_sel_hi:[0,1,1]
	s_waitcnt vmcnt(31)
	v_lshlrev_b32_e32 v0, 16, v41
	v_mul_f32_e32 v0, v46, v0
	v_and_b32_e32 v1, 0xffff0000, v41
	v_mul_f32_e32 v1, v46, v1
	v_cvt_pk_bf16_f32 v41, v0, v1
	s_waitcnt vmcnt(29)
	v_lshlrev_b32_e32 v0, 16, v45
	v_mul_f32_e32 v0, v47, v0
	v_and_b32_e32 v1, 0xffff0000, v45
	v_mul_f32_e32 v1, v47, v1
	v_cvt_pk_bf16_f32 v45, v0, v1
	s_waitcnt vmcnt(27)
	v_lshlrev_b32_e32 v0, 16, v68
	v_mul_f32_e32 v0, v48, v0
	v_and_b32_e32 v1, 0xffff0000, v68
	v_mul_f32_e32 v1, v48, v1
	v_cvt_pk_bf16_f32 v68, v0, v1
	s_waitcnt vmcnt(25)
	v_lshlrev_b32_e32 v0, 16, v69
	v_mul_f32_e32 v0, v49, v0
	v_and_b32_e32 v1, 0xffff0000, v69
	v_mul_f32_e32 v1, v49, v1
	v_cvt_pk_bf16_f32 v69, v0, v1
	s_waitcnt vmcnt(23)
	v_lshlrev_b32_e32 v0, 16, v75
	v_mul_f32_e32 v0, v50, v0
	v_and_b32_e32 v1, 0xffff0000, v75
	v_mul_f32_e32 v1, v50, v1
	v_cvt_pk_bf16_f32 v75, v0, v1
	s_waitcnt vmcnt(21)
	v_lshlrev_b32_e32 v0, 16, v77
	v_mul_f32_e32 v0, v51, v0
	v_and_b32_e32 v1, 0xffff0000, v77
	v_mul_f32_e32 v1, v51, v1
	v_cvt_pk_bf16_f32 v77, v0, v1
	s_waitcnt vmcnt(19)
	v_lshlrev_b32_e32 v0, 16, v78
	v_mul_f32_e32 v0, v52, v0
	v_and_b32_e32 v1, 0xffff0000, v78
	v_mul_f32_e32 v1, v52, v1
	v_cvt_pk_bf16_f32 v81, v0, v1
	s_waitcnt vmcnt(17)
	v_lshlrev_b32_e32 v0, 16, v79
	v_mul_f32_e32 v0, v53, v0
	v_and_b32_e32 v1, 0xffff0000, v79
	v_pk_fma_f32 v[38:39], v[8:9], v[2:3], v[82:83] op_sel_hi:[0,1,1]
	v_mul_f32_e32 v1, v53, v1
	v_cvt_pk_bf16_f32 v82, v0, v1
	v_and_b32_e32 v0, 0xffff, v41
	v_lshrrev_b32_e32 v41, 16, v41
	v_and_or_b32 v78, v45, s95, v41
	v_lshrrev_b32_e32 v41, 16, v68
	v_and_b32_e32 v1, 0xffff, v68
	v_and_b32_e32 v2, 0xffff, v75
	v_and_b32_e32 v3, 0xffff, v81
	v_and_or_b32 v79, v69, s95, v41
	v_lshrrev_b32_e32 v41, 16, v75
	v_lshl_or_b32 v0, v45, 16, v0
	v_lshl_or_b32 v1, v69, 16, v1
	v_lshl_or_b32 v2, v77, 16, v2
	v_lshl_or_b32 v3, v82, 16, v3
	v_and_or_b32 v80, v77, s95, v41
	v_lshrrev_b32_e32 v41, 16, v81
	v_and_or_b32 v81, v82, s95, v41
	ds_write_b128 v171, v[0:3] offset:32768
	ds_write_b128 v171, v[78:81] offset:32832
	v_and_b32_e32 v0, 0xffff, v4
	v_lshrrev_b32_e32 v4, 16, v4
	v_lshl_or_b32 v0, v5, 16, v0
	v_and_b32_e32 v1, 0xffff, v6
	v_and_b32_e32 v2, 0xffff, v40
	v_and_b32_e32 v3, 0xffff, v67
	v_and_or_b32 v4, v5, s95, v4
	v_lshrrev_b32_e32 v5, 16, v6
	v_lshl_or_b32 v1, v7, 16, v1
	v_lshl_or_b32 v2, v44, 16, v2
	s_waitcnt vmcnt(16)
	v_lshl_or_b32 v3, v74, 16, v3
	v_and_or_b32 v5, v7, s95, v5
	v_lshrrev_b32_e32 v6, 16, v40
	v_lshrrev_b32_e32 v7, 16, v67
	v_and_or_b32 v6, v44, s95, v6
	v_and_or_b32 v7, v74, s95, v7
	ds_write_b128 v171, v[0:3] offset:49152
	ds_write_b128 v171, v[4:7] offset:49216
	s_waitcnt lgkmcnt(0)
	s_barrier
	ds_read_b128 v[0:3], v172 offset:32768
	ds_read_b128 v[4:7], v172 offset:33792
	ds_read_b128 v[244:247], v170 offset:49152
	ds_read_b128 v[248:251], v170 offset:50176
	ds_read_b128 v[252:255], v170 offset:51200
	ds_read_b128 v[196:199], v170 offset:52224
	s_waitcnt lgkmcnt(3)
	v_mfma_f32_16x16x32_bf16 v[78:81], v[0:3], v[244:247], 0
	s_waitcnt lgkmcnt(2)
	v_mfma_f32_16x16x32_bf16 v[78:81], v[4:7], v[248:251], v[78:81]
	ds_read_b128 v[244:247], v170 offset:53248
	ds_read_b128 v[248:251], v170 offset:54272
	s_nop 7
	v_pk_fma_f32 v[14:15], v[8:9], v[14:15], v[78:79] op_sel_hi:[0,1,1]
	v_pk_fma_f32 v[26:27], v[8:9], v[26:27], v[80:81] op_sel_hi:[0,1,1]
	s_waitcnt lgkmcnt(3)
	v_mfma_f32_16x16x32_bf16 v[78:81], v[0:3], v[252:255], 0
	s_waitcnt lgkmcnt(2)
	v_mfma_f32_16x16x32_bf16 v[78:81], v[4:7], v[196:199], v[78:81]
	ds_read_b128 v[252:255], v170 offset:55296
	ds_read_b128 v[196:199], v170 offset:56320
	s_nop 7
	v_pk_fma_f32 v[16:17], v[8:9], v[16:17], v[78:79] op_sel_hi:[0,1,1]
	v_pk_fma_f32 v[28:29], v[8:9], v[28:29], v[80:81] op_sel_hi:[0,1,1]
	s_waitcnt lgkmcnt(3)
	v_mfma_f32_16x16x32_bf16 v[78:81], v[0:3], v[244:247], 0
	s_waitcnt lgkmcnt(2)
	v_mfma_f32_16x16x32_bf16 v[78:81], v[4:7], v[248:251], v[78:81]
	ds_read_b128 v[244:247], v170 offset:57344
	ds_read_b128 v[248:251], v170 offset:58368
	s_nop 7
	v_pk_fma_f32 v[18:19], v[8:9], v[18:19], v[78:79] op_sel_hi:[0,1,1]
	v_pk_fma_f32 v[30:31], v[8:9], v[30:31], v[80:81] op_sel_hi:[0,1,1]
	s_waitcnt lgkmcnt(3)
	v_mfma_f32_16x16x32_bf16 v[78:81], v[0:3], v[252:255], 0
	s_waitcnt lgkmcnt(2)
	v_mfma_f32_16x16x32_bf16 v[78:81], v[4:7], v[196:199], v[78:81]
	ds_read_b128 v[252:255], v170 offset:59392
	ds_read_b128 v[196:199], v170 offset:60416
	s_nop 7
	v_pk_fma_f32 v[20:21], v[8:9], v[20:21], v[78:79] op_sel_hi:[0,1,1]
	v_pk_fma_f32 v[32:33], v[8:9], v[32:33], v[80:81] op_sel_hi:[0,1,1]
	s_waitcnt lgkmcnt(3)
	v_mfma_f32_16x16x32_bf16 v[78:81], v[0:3], v[244:247], 0
	s_waitcnt lgkmcnt(2)
	v_mfma_f32_16x16x32_bf16 v[78:81], v[4:7], v[248:251], v[78:81]
	ds_read_b128 v[244:247], v170 offset:61440
	ds_read_b128 v[248:251], v170 offset:62464
	s_nop 7
	v_pk_fma_f32 v[22:23], v[8:9], v[22:23], v[78:79] op_sel_hi:[0,1,1]
	v_pk_fma_f32 v[34:35], v[8:9], v[34:35], v[80:81] op_sel_hi:[0,1,1]
	s_waitcnt lgkmcnt(3)
	v_mfma_f32_16x16x32_bf16 v[78:81], v[0:3], v[252:255], 0
	s_waitcnt lgkmcnt(2)
	v_mfma_f32_16x16x32_bf16 v[78:81], v[4:7], v[196:199], v[78:81]
	ds_read_b128 v[252:255], v170 offset:63488
	ds_read_b128 v[196:199], v170 offset:64512
	s_nop 7
	v_pk_fma_f32 v[24:25], v[8:9], v[24:25], v[78:79] op_sel_hi:[0,1,1]
	v_pk_fma_f32 v[36:37], v[8:9], v[36:37], v[80:81] op_sel_hi:[0,1,1]
	s_waitcnt lgkmcnt(3)
	v_mfma_f32_16x16x32_bf16 v[78:81], v[0:3], v[244:247], 0
	s_waitcnt lgkmcnt(2)
	v_mfma_f32_16x16x32_bf16 v[78:81], v[4:7], v[248:251], v[78:81]
	s_nop 7
	v_pk_fma_f32 v[40:41], v[8:9], v[12:13], v[78:79] op_sel_hi:[0,1,1]
	v_pk_fma_f32 v[44:45], v[8:9], v[10:11], v[80:81] op_sel_hi:[0,1,1]
	s_waitcnt lgkmcnt(1)
	v_mfma_f32_16x16x32_bf16 v[0:3], v[0:3], v[252:255], 0
	s_waitcnt lgkmcnt(0)
	v_mfma_f32_16x16x32_bf16 v[0:3], v[4:7], v[196:199], v[0:3]
	s_nop 7
	v_pk_fma_f32 v[10:11], v[8:9], v[42:43], v[0:1] op_sel_hi:[0,1,1]
	s_waitcnt vmcnt(15)
	v_lshlrev_b32_e32 v0, 16, v59
	v_mul_f32_e32 v0, v46, v0
	v_and_b32_e32 v1, 0xffff0000, v59
	v_mul_f32_e32 v1, v46, v1
	v_cvt_pk_bf16_f32 v4, v0, v1
	s_waitcnt vmcnt(13)
	v_lshlrev_b32_e32 v0, 16, v61
	v_mul_f32_e32 v0, v47, v0
	v_and_b32_e32 v1, 0xffff0000, v61
	v_mul_f32_e32 v1, v47, v1
	v_cvt_pk_bf16_f32 v5, v0, v1
	s_waitcnt vmcnt(11)
	v_lshlrev_b32_e32 v0, 16, v63
	v_mul_f32_e32 v0, v48, v0
	v_and_b32_e32 v1, 0xffff0000, v63
	v_mul_f32_e32 v1, v48, v1
	v_cvt_pk_bf16_f32 v6, v0, v1
	s_waitcnt vmcnt(9)
	v_lshlrev_b32_e32 v0, 16, v66
	v_mul_f32_e32 v0, v49, v0
	v_and_b32_e32 v1, 0xffff0000, v66
	v_mul_f32_e32 v1, v49, v1
	v_cvt_pk_bf16_f32 v7, v0, v1
	s_waitcnt vmcnt(7)
	v_lshlrev_b32_e32 v0, 16, v71
	v_mul_f32_e32 v0, v50, v0
	v_and_b32_e32 v1, 0xffff0000, v71
	v_pk_fma_f32 v[12:13], v[8:9], v[38:39], v[2:3] op_sel_hi:[0,1,1]
	v_mul_f32_e32 v1, v50, v1
	v_cvt_pk_bf16_f32 v38, v0, v1
	s_waitcnt vmcnt(5)
	v_lshlrev_b32_e32 v0, 16, v72
	v_mul_f32_e32 v0, v51, v0
	v_and_b32_e32 v1, 0xffff0000, v72
	v_mul_f32_e32 v1, v51, v1
	v_cvt_pk_bf16_f32 v39, v0, v1
	s_waitcnt vmcnt(3)
	v_lshlrev_b32_e32 v0, 16, v73
	v_mul_f32_e32 v0, v52, v0
	v_and_b32_e32 v1, 0xffff0000, v73
	v_mul_f32_e32 v1, v52, v1
	v_cvt_pk_bf16_f32 v42, v0, v1
	s_waitcnt vmcnt(1)
	v_lshlrev_b32_e32 v0, 16, v76
	v_mul_f32_e32 v0, v53, v0
	v_and_b32_e32 v1, 0xffff0000, v76
	v_mul_f32_e32 v1, v53, v1
	v_cvt_pk_bf16_f32 v43, v0, v1
	v_and_b32_e32 v0, 0xffff, v4
	v_lshrrev_b32_e32 v4, 16, v4
	v_lshl_or_b32 v0, v5, 16, v0
	v_and_b32_e32 v1, 0xffff, v6
	v_and_b32_e32 v2, 0xffff, v38
	v_and_b32_e32 v3, 0xffff, v42
	v_and_or_b32 v4, v5, s95, v4
	v_lshrrev_b32_e32 v5, 16, v6
	v_lshl_or_b32 v1, v7, 16, v1
	v_lshl_or_b32 v2, v39, 16, v2
	v_lshl_or_b32 v3, v43, 16, v3
	v_and_or_b32 v5, v7, s95, v5
	v_lshrrev_b32_e32 v6, 16, v38
	v_lshrrev_b32_e32 v7, 16, v42
	v_and_or_b32 v6, v39, s95, v6
	v_and_or_b32 v7, v43, s95, v7
	ds_write_b128 v171, v[0:3]
	ds_write_b128 v171, v[4:7] offset:64
	v_and_b32_e32 v0, 0xffff, v54
	v_and_b32_e32 v1, 0xffff, v56
	v_and_b32_e32 v2, 0xffff, v58
	v_and_b32_e32 v3, 0xffff, v62
	v_lshl_or_b32 v0, v55, 16, v0
	v_lshl_or_b32 v1, v57, 16, v1
	v_lshl_or_b32 v2, v60, 16, v2
	s_waitcnt vmcnt(0)
	v_lshl_or_b32 v3, v70, 16, v3
	v_lshrrev_b32_e32 v4, 16, v54
	v_lshrrev_b32_e32 v5, 16, v56
	v_lshrrev_b32_e32 v6, 16, v58
	v_lshrrev_b32_e32 v7, 16, v62
	v_and_or_b32 v4, v55, s95, v4
	v_and_or_b32 v5, v57, s95, v5
	v_and_or_b32 v6, v60, s95, v6
	v_and_or_b32 v7, v70, s95, v7
	ds_write_b128 v171, v[0:3] offset:16384
	ds_write_b128 v171, v[4:7] offset:16448
	s_waitcnt lgkmcnt(0)
	s_barrier
	ds_read_b128 v[4:7], v172
	ds_read_b128 v[0:3], v172 offset:1024
	ds_read_b128 v[244:247], v170 offset:16384
	ds_read_b128 v[248:251], v170 offset:17408
	ds_read_b128 v[252:255], v170 offset:18432
	ds_read_b128 v[196:199], v170 offset:19456
	s_waitcnt lgkmcnt(3)
	v_mfma_f32_16x16x32_bf16 v[46:49], v[4:7], v[244:247], 0
	s_waitcnt lgkmcnt(2)
	v_mfma_f32_16x16x32_bf16 v[46:49], v[0:3], v[248:251], v[46:49]
	ds_read_b128 v[244:247], v170 offset:20480
	ds_read_b128 v[248:251], v170 offset:21504
	s_nop 7
	v_pk_fma_f32 v[26:27], v[8:9], v[26:27], v[48:49] op_sel_hi:[0,1,1]
	v_pk_fma_f32 v[14:15], v[8:9], v[14:15], v[46:47] op_sel_hi:[0,1,1]
	s_waitcnt lgkmcnt(3)
	v_mfma_f32_16x16x32_bf16 v[46:49], v[4:7], v[252:255], 0
	s_waitcnt lgkmcnt(2)
	v_mfma_f32_16x16x32_bf16 v[46:49], v[0:3], v[196:199], v[46:49]
	ds_read_b128 v[252:255], v170 offset:22528
	ds_read_b128 v[196:199], v170 offset:23552
	s_nop 7
	v_pk_fma_f32 v[28:29], v[8:9], v[28:29], v[48:49] op_sel_hi:[0,1,1]
	v_pk_fma_f32 v[16:17], v[8:9], v[16:17], v[46:47] op_sel_hi:[0,1,1]
	s_waitcnt lgkmcnt(3)
	v_mfma_f32_16x16x32_bf16 v[46:49], v[4:7], v[244:247], 0
	s_waitcnt lgkmcnt(2)
	v_mfma_f32_16x16x32_bf16 v[46:49], v[0:3], v[248:251], v[46:49]
	ds_read_b128 v[244:247], v170 offset:24576
	ds_read_b128 v[248:251], v170 offset:25600
	s_nop 7
	v_pk_fma_f32 v[38:39], v[8:9], v[30:31], v[48:49] op_sel_hi:[0,1,1]
	v_pk_fma_f32 v[42:43], v[8:9], v[18:19], v[46:47] op_sel_hi:[0,1,1]
	s_waitcnt lgkmcnt(3)
	v_mfma_f32_16x16x32_bf16 v[46:49], v[4:7], v[252:255], 0
	s_waitcnt lgkmcnt(2)
	v_mfma_f32_16x16x32_bf16 v[46:49], v[0:3], v[196:199], v[46:49]
	ds_read_b128 v[252:255], v170 offset:26624
	ds_read_b128 v[196:199], v170 offset:27648
	s_nop 7
	v_pk_fma_f32 v[48:49], v[8:9], v[32:33], v[48:49] op_sel_hi:[0,1,1]
	v_pk_fma_f32 v[46:47], v[8:9], v[20:21], v[46:47] op_sel_hi:[0,1,1]
	s_waitcnt lgkmcnt(3)
	v_mfma_f32_16x16x32_bf16 v[18:21], v[4:7], v[244:247], 0
	s_waitcnt lgkmcnt(2)
	v_mfma_f32_16x16x32_bf16 v[18:21], v[0:3], v[248:251], v[18:21]
	ds_read_b128 v[244:247], v170 offset:28672
	ds_read_b128 v[248:251], v170 offset:29696
	s_nop 7
	v_pk_fma_f32 v[34:35], v[8:9], v[34:35], v[20:21] op_sel_hi:[0,1,1]
	v_pk_fma_f32 v[50:51], v[8:9], v[22:23], v[18:19] op_sel_hi:[0,1,1]
	s_waitcnt lgkmcnt(3)
	v_mfma_f32_16x16x32_bf16 v[18:21], v[4:7], v[252:255], 0
	s_waitcnt lgkmcnt(2)
	v_mfma_f32_16x16x32_bf16 v[18:21], v[0:3], v[196:199], v[18:21]
	ds_read_b128 v[252:255], v170 offset:30720
	ds_read_b128 v[196:199], v170 offset:31744
	s_nop 7
	v_pk_fma_f32 v[30:31], v[8:9], v[36:37], v[20:21] op_sel_hi:[0,1,1]
	v_pk_fma_f32 v[32:33], v[8:9], v[24:25], v[18:19] op_sel_hi:[0,1,1]
	s_waitcnt lgkmcnt(3)
	v_mfma_f32_16x16x32_bf16 v[18:21], v[4:7], v[244:247], 0
	s_waitcnt lgkmcnt(2)
	v_mfma_f32_16x16x32_bf16 v[18:21], v[0:3], v[248:251], v[18:21]
	s_nop 7
	v_pk_fma_f32 v[36:37], v[8:9], v[44:45], v[20:21] op_sel_hi:[0,1,1]
	v_pk_fma_f32 v[40:41], v[8:9], v[40:41], v[18:19] op_sel_hi:[0,1,1]
	s_waitcnt lgkmcnt(1)
	v_mfma_f32_16x16x32_bf16 v[4:7], v[4:7], v[252:255], 0
	s_waitcnt lgkmcnt(0)
	v_mfma_f32_16x16x32_bf16 v[0:3], v[0:3], v[196:199], v[4:7]
	v_cvt_pk_bf16_f32 v4, v14, v15
	v_cvt_pk_bf16_f32 v5, v26, v27
	s_nop 5
	v_lshl_add_u64 v[6:7], s[40:41], 0, v[124:125]
	global_store_dwordx2 v[6:7], v[4:5], off
	v_lshl_add_u64 v[6:7], s[40:41], 0, v[126:127]
	v_cvt_pk_bf16_f32 v4, v16, v17
	v_cvt_pk_bf16_f32 v5, v28, v29
	global_store_dwordx2 v[6:7], v[4:5], off
	v_lshl_add_u64 v[6:7], s[40:41], 0, v[128:129]
	v_cvt_pk_bf16_f32 v4, v42, v43
	v_cvt_pk_bf16_f32 v5, v38, v39
	global_store_dwordx2 v[6:7], v[4:5], off
	v_lshl_add_u64 v[6:7], s[40:41], 0, v[130:131]
	v_cvt_pk_bf16_f32 v4, v46, v47
	v_cvt_pk_bf16_f32 v5, v48, v49
	global_store_dwordx2 v[6:7], v[4:5], off
	v_lshl_add_u64 v[6:7], s[40:41], 0, v[132:133]
	v_cvt_pk_bf16_f32 v4, v50, v51
	v_cvt_pk_bf16_f32 v5, v34, v35
	global_store_dwordx2 v[6:7], v[4:5], off
	v_lshl_add_u64 v[6:7], s[40:41], 0, v[134:135]
	v_pk_fma_f32 v[2:3], v[8:9], v[12:13], v[2:3] op_sel_hi:[0,1,1]
	v_pk_fma_f32 v[0:1], v[8:9], v[10:11], v[0:1] op_sel_hi:[0,1,1]
	v_cvt_pk_bf16_f32 v4, v32, v33
	v_cvt_pk_bf16_f32 v5, v30, v31
	global_store_dwordx2 v[6:7], v[4:5], off
	v_lshl_add_u64 v[6:7], s[40:41], 0, v[136:137]
	v_cvt_pk_bf16_f32 v4, v40, v41
	v_cvt_pk_bf16_f32 v5, v36, v37
	global_store_dwordx2 v[6:7], v[4:5], off
	v_cvt_pk_bf16_f32 v0, v0, v1
	v_cvt_pk_bf16_f32 v1, v2, v3
	v_lshl_add_u64 v[2:3], s[40:41], 0, v[138:139]
	s_mov_b64 s[40:41], 0
	global_store_dwordx2 v[2:3], v[0:1], off
	s_cbranch_vccz .LBB0_475
	v_mul_f32_e32 v0, 0xc3800000, v9
	v_mul_f32_e32 v0, 0x3fb8aa3b, v0
	v_exp_f32_e32 v0, v0
	s_mov_b64 s[40:41], -1
	v_mov_b32_e32 v1, v0
	s_branch .LBB0_475

.LBB0_556:
	s_and_b32 s24, s58, 63
	s_cmp_lg_u32 s24, 0
	v_readlane_b32 s26, v241, 10
	s_cselect_b64 s[20:21], -1, 0
	v_readlane_b32 s27, v241, 11
	s_or_b64 s[26:27], s[26:27], s[20:21]
	s_andn2_b64 vcc, exec, s[26:27]
	s_cbranch_vccnz .LBB0_555
	s_ashr_i32 s26, s58, 6
	s_and_b32 s25, s58, 64
	s_sub_i32 s27, 0x41, s24
	s_and_b64 s[20:21], s[20:21], exec
	s_cselect_b32 s20, s27, 0
	s_cmp_eq_u32 s25, 0
	s_cselect_b32 s24, s24, s20
	s_bitcmp0_b32 s58, 9
	v_add_u32_e32 v170, s53, v64
	s_mul_i32 s25, s26, 0x41
	s_cbranch_scc1 .LBB0_560
	s_bfe_u32 s61, s58, 0x10006
	s_bfe_u32 s21, s26, 0x20001
	s_lshl_b32 s26, s21, 2
	s_lshl_b32 s27, s61, 4
	s_or_b32 s26, s27, s26
	v_mov_b32_e32 v0, s26
	v_readlane_b32 s26, v241, 6
	v_readlane_b32 s27, v241, 7
	s_bfe_i32 s20, s58, 0x10006
	s_lshl_b32 s39, s24, 8
	s_and_b32 s20, s20, 0xc0
	s_lshl_b32 s63, s21, 8
	s_nop 0
	global_load_dword v0, v0, s[26:27]
	s_mov_b32 s26, 0xc2ce8ed0
	s_waitcnt vmcnt(0)
	v_mul_f32_e32 v1, 0x3fb8aa3b, v0
	v_fma_f32 v2, v0, s94, -v1
	v_rndne_f32_e32 v3, v1
	v_fmac_f32_e32 v2, 0x32a5705f, v0
	v_sub_f32_e32 v1, v1, v3
	v_add_f32_e32 v1, v1, v2
	v_exp_f32_e32 v1, v1
	v_cvt_i32_f32_e32 v2, v3
	v_cmp_ngt_f32_e32 vcc, s26, v0
	s_mov_b32 s26, 0x42b17218
	v_ldexp_f32 v1, v1, v2
	v_cndmask_b32_e32 v1, 0, v1, vcc
	v_cmp_nlt_f32_e32 vcc, s26, v0
	s_ashr_i32 s26, s58, 10
	s_mulk_i32 s26, 0x4100
	s_add_i32 s39, s39, s26
	s_or_b32 s62, s39, s20
	v_cndmask_b32_e32 v9, v204, v1, vcc
	s_cmp_eq_u32 s61, 0
	v_mul_f32_e32 v0, 0xc2800000, v9
	s_cselect_b32 s59, s2, s3
	v_mul_f32_e32 v0, 0x3fb8aa3b, v0
	s_cselect_b32 s38, s33, s40
	s_cselect_b32 s37, s41, s42
	s_cselect_b32 s36, s43, s44
	s_cselect_b32 s35, s45, s46
	s_cselect_b32 s34, s47, s48
	s_cselect_b32 s27, s49, s50
	s_cselect_b32 s26, s51, s52
	s_cselect_b32 s60, 0xc0, 0
	s_add_i32 s20, s62, s59
	v_exp_f32_e32 v8, v0
	v_mad_i64_i32 v[0:1], s[20:21], s20, v205, v[126:127]
	s_or_b32 s78, s63, 0x1800
	v_lshl_add_u64 v[2:3], v[0:1], 0, s[78:79]
	global_load_dword v3, v[2:3], off
	s_or_b32 s20, s63, 0x1c00
	s_add_i32 s63, s62, s38
	v_mad_i64_i32 v[4:5], s[64:65], s63, v205, v[126:127]
	v_lshl_add_u64 v[6:7], v[4:5], 0, s[78:79]
	global_load_dword v30, v[6:7], off
	s_mov_b32 s21, s79
	v_lshl_add_u64 v[0:1], v[0:1], 0, s[20:21]
	v_lshl_add_u64 v[4:5], v[4:5], 0, s[20:21]
	s_add_i32 s63, s62, s37
	global_load_dword v0, v[0:1], off
	s_lshl_b32 s61, s61, 6
	global_load_dword v1, v[4:5], off
	v_mad_i64_i32 v[4:5], s[64:65], s63, v205, v[126:127]
	v_lshl_add_u64 v[6:7], v[4:5], 0, s[78:79]
	global_load_dword v31, v[6:7], off
	v_lshl_add_u64 v[4:5], v[4:5], 0, s[20:21]
	s_add_i32 s63, s62, s36
	global_load_dword v2, v[4:5], off
	v_mad_i64_i32 v[4:5], s[64:65], s63, v205, v[126:127]
	v_lshl_add_u64 v[6:7], v[4:5], 0, s[78:79]
	global_load_dword v32, v[6:7], off
	v_lshl_add_u64 v[4:5], v[4:5], 0, s[20:21]
	s_add_i32 s63, s62, s35
	global_load_dword v14, v[4:5], off
	v_mad_i64_i32 v[4:5], s[64:65], s63, v205, v[126:127]
	v_lshl_add_u64 v[6:7], v[4:5], 0, s[78:79]
	global_load_dword v33, v[6:7], off
	v_lshl_add_u64 v[4:5], v[4:5], 0, s[20:21]
	s_add_i32 s63, s62, s34
	global_load_dword v21, v[4:5], off
	v_mad_i64_i32 v[4:5], s[64:65], s63, v205, v[126:127]
	v_lshl_add_u64 v[6:7], v[4:5], 0, s[78:79]
	global_load_dword v34, v[6:7], off
	v_lshl_add_u64 v[4:5], v[4:5], 0, s[20:21]
	s_add_i32 s63, s62, s27
	global_load_dword v23, v[4:5], off
	v_mad_i64_i32 v[4:5], s[64:65], s63, v205, v[126:127]
	v_lshl_add_u64 v[6:7], v[4:5], 0, s[78:79]
	v_lshl_add_u64 v[4:5], v[4:5], 0, s[20:21]
	s_add_i32 s62, s62, s26
	global_load_dword v35, v[6:7], off
	global_load_dword v28, v[4:5], off
	v_mad_i64_i32 v[4:5], s[62:63], s62, v205, v[126:127]
	s_or_b32 s62, s61, s39
	s_add_i32 s64, s62, 64
	v_lshl_add_u64 v[6:7], v[4:5], 0, s[78:79]
	v_lshl_add_u64 v[4:5], v[4:5], 0, s[20:21]
	s_add_i32 s62, s64, s59
	global_load_dword v36, v[6:7], off
	global_load_dword v37, v[4:5], off
	v_mad_i64_i32 v[4:5], s[62:63], s62, v205, v[126:127]
	v_lshl_add_u64 v[6:7], v[4:5], 0, s[78:79]
	v_lshl_add_u64 v[4:5], v[4:5], 0, s[20:21]
	s_add_i32 s62, s64, s38
	global_load_dword v16, v[6:7], off
	global_load_dword v10, v[4:5], off
	v_mad_i64_i32 v[4:5], s[62:63], s62, v205, v[126:127]
	v_lshl_add_u64 v[6:7], v[4:5], 0, s[78:79]
	v_lshl_add_u64 v[4:5], v[4:5], 0, s[20:21]
	s_add_i32 s62, s64, s37
	global_load_dword v18, v[6:7], off
	global_load_dword v11, v[4:5], off
	v_mad_i64_i32 v[4:5], s[62:63], s62, v205, v[126:127]
	v_lshl_add_u64 v[6:7], v[4:5], 0, s[78:79]
	v_lshl_add_u64 v[4:5], v[4:5], 0, s[20:21]
	s_add_i32 s62, s64, s36
	global_load_dword v20, v[6:7], off
	global_load_dword v12, v[4:5], off
	v_mad_i64_i32 v[4:5], s[62:63], s62, v205, v[126:127]
	v_lshl_add_u64 v[6:7], v[4:5], 0, s[78:79]
	v_lshl_add_u64 v[4:5], v[4:5], 0, s[20:21]
	s_add_i32 s62, s64, s35
	global_load_dword v22, v[6:7], off
	global_load_dword v13, v[4:5], off
	v_mad_i64_i32 v[4:5], s[62:63], s62, v205, v[126:127]
	v_lshl_add_u64 v[6:7], v[4:5], 0, s[78:79]
	v_lshl_add_u64 v[4:5], v[4:5], 0, s[20:21]
	s_add_i32 s62, s64, s34
	global_load_dword v25, v[6:7], off
	global_load_dword v15, v[4:5], off
	v_mad_i64_i32 v[4:5], s[62:63], s62, v205, v[126:127]
	v_lshl_add_u64 v[6:7], v[4:5], 0, s[78:79]
	v_lshl_add_u64 v[4:5], v[4:5], 0, s[20:21]
	s_add_i32 s62, s64, s27
	global_load_dword v26, v[6:7], off
	global_load_dword v17, v[4:5], off
	v_mad_i64_i32 v[4:5], s[62:63], s62, v205, v[126:127]
	v_lshl_add_u64 v[6:7], v[4:5], 0, s[78:79]
	v_lshl_add_u64 v[4:5], v[4:5], 0, s[20:21]
	s_add_i32 s64, s64, s26
	s_sub_i32 s61, s39, s61
	global_load_dword v27, v[6:7], off
	global_load_dword v19, v[4:5], off
	v_mad_i64_i32 v[4:5], s[62:63], s64, v205, v[126:127]
	s_addk_i32 s61, 0x80
	v_lshl_add_u64 v[6:7], v[4:5], 0, s[78:79]
	v_lshl_add_u64 v[4:5], v[4:5], 0, s[20:21]
	s_add_i32 s62, s61, s59
	global_load_dword v29, v[6:7], off
	global_load_dword v24, v[4:5], off
	v_mad_i64_i32 v[4:5], s[62:63], s62, v205, v[126:127]
	v_lshl_add_u64 v[6:7], v[4:5], 0, s[78:79]
	v_lshl_add_u64 v[4:5], v[4:5], 0, s[20:21]
	s_add_i32 s62, s61, s38
	global_load_dword v41, v[6:7], off
	s_nop 0
	global_load_dword v4, v[4:5], off
	v_mad_i64_i32 v[6:7], s[62:63], s62, v205, v[126:127]
	v_lshl_add_u64 v[38:39], v[6:7], 0, s[78:79]
	v_lshl_add_u64 v[6:7], v[6:7], 0, s[20:21]
	s_add_i32 s62, s61, s37
	global_load_dword v45, v[38:39], off
	global_load_dword v5, v[6:7], off
	v_mad_i64_i32 v[6:7], s[62:63], s62, v205, v[126:127]
	v_lshl_add_u64 v[38:39], v[6:7], 0, s[78:79]
	v_lshl_add_u64 v[6:7], v[6:7], 0, s[20:21]
	s_add_i32 s62, s61, s36
	global_load_dword v68, v[38:39], off
	s_nop 0
	global_load_dword v6, v[6:7], off
	v_mad_i64_i32 v[38:39], s[62:63], s62, v205, v[126:127]
	v_lshl_add_u64 v[42:43], v[38:39], 0, s[78:79]
	v_lshl_add_u64 v[38:39], v[38:39], 0, s[20:21]
	s_add_i32 s62, s61, s35
	global_load_dword v69, v[42:43], off
	global_load_dword v7, v[38:39], off
	v_mad_i64_i32 v[38:39], s[62:63], s62, v205, v[126:127]
	v_lshl_add_u64 v[42:43], v[38:39], 0, s[78:79]
	v_lshl_add_u64 v[38:39], v[38:39], 0, s[20:21]
	s_add_i32 s62, s61, s34
	global_load_dword v75, v[42:43], off
	global_load_dword v40, v[38:39], off
	v_mad_i64_i32 v[38:39], s[62:63], s62, v205, v[126:127]
	v_lshl_add_u64 v[42:43], v[38:39], 0, s[78:79]
	v_lshl_add_u64 v[38:39], v[38:39], 0, s[20:21]
	s_add_i32 s62, s61, s27
	global_load_dword v77, v[42:43], off
	global_load_dword v44, v[38:39], off
	v_mad_i64_i32 v[38:39], s[62:63], s62, v205, v[126:127]
	v_lshl_add_u64 v[42:43], v[38:39], 0, s[78:79]
	v_lshl_add_u64 v[38:39], v[38:39], 0, s[20:21]
	s_add_i32 s61, s61, s26
	global_load_dword v78, v[42:43], off
	global_load_dword v67, v[38:39], off
	v_mad_i64_i32 v[38:39], s[62:63], s61, v205, v[126:127]
	v_lshl_add_u64 v[42:43], v[38:39], 0, s[78:79]
	v_lshl_add_u64 v[38:39], v[38:39], 0, s[20:21]
	global_load_dword v79, v[42:43], off
	global_load_dword v74, v[38:39], off
	v_mul_f32_e64 v38, v162, -v9
	v_mul_f32_e32 v38, 0x3fb8aa3b, v38
	v_exp_f32_e32 v46, v38
	s_waitcnt vmcnt(47)
	v_lshlrev_b32_e32 v38, 16, v3
	v_and_b32_e32 v3, 0xffff0000, v3
	s_waitcnt lgkmcnt(0)
	v_mul_f32_e32 v38, v46, v38
	v_mul_f32_e32 v3, v46, v3
	s_barrier
	v_cvt_pk_bf16_f32 v3, v38, v3
	v_mul_f32_e64 v38, v163, -v9
	v_mul_f32_e32 v38, 0x3fb8aa3b, v38
	v_exp_f32_e32 v47, v38
	s_waitcnt vmcnt(46)
	v_lshlrev_b32_e32 v38, 16, v30
	v_and_b32_e32 v30, 0xffff0000, v30
	s_or_b32 s62, s39, s60
	v_mul_f32_e32 v38, v47, v38
	v_mul_f32_e32 v30, v47, v30
	v_cvt_pk_bf16_f32 v38, v38, v30
	v_mul_f32_e64 v30, v164, -v9
	v_mul_f32_e32 v30, 0x3fb8aa3b, v30
	v_exp_f32_e32 v48, v30
	s_waitcnt vmcnt(43)
	v_lshlrev_b32_e32 v30, 16, v31
	v_and_b32_e32 v31, 0xffff0000, v31
	s_add_i32 s39, s62, s59
	v_mul_f32_e32 v30, v48, v30
	v_mul_f32_e32 v31, v48, v31
	v_cvt_pk_bf16_f32 v39, v30, v31
	v_mul_f32_e64 v30, v165, -v9
	v_mul_f32_e32 v30, 0x3fb8aa3b, v30
	v_exp_f32_e32 v49, v30
	s_waitcnt vmcnt(41)
	v_lshlrev_b32_e32 v30, 16, v32
	v_and_b32_e32 v31, 0xffff0000, v32
	s_add_i32 s38, s62, s38
	v_mul_f32_e32 v30, v49, v30
	v_mul_f32_e32 v31, v49, v31
	v_cvt_pk_bf16_f32 v42, v30, v31
	v_mul_f32_e64 v30, v166, -v9
	v_mul_f32_e32 v30, 0x3fb8aa3b, v30
	v_exp_f32_e32 v50, v30
	s_waitcnt vmcnt(39)
	v_lshlrev_b32_e32 v30, 16, v33
	v_and_b32_e32 v31, 0xffff0000, v33
	s_add_i32 s37, s62, s37
	v_mul_f32_e32 v30, v50, v30
	v_mul_f32_e32 v31, v50, v31
	v_cvt_pk_bf16_f32 v43, v30, v31
	v_mul_f32_e64 v30, v167, -v9
	v_mul_f32_e32 v30, 0x3fb8aa3b, v30
	v_exp_f32_e32 v51, v30
	s_waitcnt vmcnt(37)
	v_lshlrev_b32_e32 v30, 16, v34
	v_and_b32_e32 v31, 0xffff0000, v34
	v_and_b32_e32 v32, 0xffff, v43
	v_mul_f32_e32 v30, v51, v30
	v_mul_f32_e32 v31, v51, v31
	v_cvt_pk_bf16_f32 v34, v30, v31
	v_mul_f32_e64 v30, v168, -v9
	v_mul_f32_e32 v30, 0x3fb8aa3b, v30
	v_exp_f32_e32 v52, v30
	s_waitcnt vmcnt(35)
	v_lshlrev_b32_e32 v30, 16, v35
	v_and_b32_e32 v31, 0xffff0000, v35
	v_lshl_or_b32 v32, v34, 16, v32
	v_mul_f32_e32 v30, v52, v30
	v_mul_f32_e32 v31, v52, v31
	v_cvt_pk_bf16_f32 v35, v30, v31
	v_mul_f32_e64 v30, v169, -v9
	v_mul_f32_e32 v30, 0x3fb8aa3b, v30
	v_exp_f32_e32 v53, v30
	s_waitcnt vmcnt(33)
	v_lshlrev_b32_e32 v30, 16, v36
	v_and_b32_e32 v31, 0xffff0000, v36
	v_and_b32_e32 v33, 0xffff, v35
	v_mul_f32_e32 v30, v53, v30
	v_mul_f32_e32 v31, v53, v31
	v_cvt_pk_bf16_f32 v36, v30, v31
	v_and_b32_e32 v30, 0xffff, v3
	v_lshrrev_b32_e32 v3, 16, v3
	v_and_or_b32 v54, v38, s95, v3
	v_lshrrev_b32_e32 v3, 16, v39
	v_and_or_b32 v55, v42, s95, v3
	v_lshrrev_b32_e32 v3, 16, v43
	v_and_b32_e32 v31, 0xffff, v39
	v_and_or_b32 v56, v34, s95, v3
	v_lshrrev_b32_e32 v3, 16, v35
	v_lshl_or_b32 v30, v38, 16, v30
	v_lshl_or_b32 v31, v42, 16, v31
	v_lshl_or_b32 v33, v36, 16, v33
	v_and_or_b32 v57, v36, s95, v3
	v_and_b32_e32 v3, 0xffff, v0
	ds_write_b128 v161, v[30:33] offset:32768
	ds_write_b128 v161, v[54:57] offset:32832
	v_lshl_or_b32 v30, v1, 16, v3
	v_and_b32_e32 v3, 0xffff, v2
	v_lshl_or_b32 v31, v14, 16, v3
	v_and_b32_e32 v3, 0xffff, v21
	v_lshrrev_b32_e32 v0, 16, v0
	v_lshl_or_b32 v32, v23, 16, v3
	v_and_b32_e32 v3, 0xffff, v28
	v_and_or_b32 v0, v1, s95, v0
	v_lshrrev_b32_e32 v1, 16, v2
	s_waitcnt vmcnt(32)
	v_lshl_or_b32 v33, v37, 16, v3
	v_and_or_b32 v1, v14, s95, v1
	v_lshrrev_b32_e32 v2, 16, v21
	v_lshrrev_b32_e32 v3, 16, v28
	v_and_or_b32 v2, v23, s95, v2
	v_and_or_b32 v3, v37, s95, v3
	ds_write_b128 v161, v[30:33] offset:49152
	ds_write_b128 v161, v[0:3] offset:49216
	v_mad_i64_i32 v[0:1], s[60:61], s39, v205, v[126:127]
	v_lshl_add_u64 v[2:3], v[0:1], 0, s[78:79]
	v_lshl_add_u64 v[0:1], v[0:1], 0, s[20:21]
	global_load_dword v59, v[2:3], off
	global_load_dword v54, v[0:1], off
	v_mad_i64_i32 v[0:1], s[38:39], s38, v205, v[126:127]
	v_lshl_add_u64 v[2:3], v[0:1], 0, s[78:79]
	v_lshl_add_u64 v[0:1], v[0:1], 0, s[20:21]
	global_load_dword v61, v[2:3], off
	global_load_dword v55, v[0:1], off
	v_mad_i64_i32 v[0:1], s[38:39], s37, v205, v[126:127]
	v_lshl_add_u64 v[2:3], v[0:1], 0, s[78:79]
	v_lshl_add_u64 v[0:1], v[0:1], 0, s[20:21]
	s_add_i32 s36, s62, s36
	global_load_dword v63, v[2:3], off
	global_load_dword v56, v[0:1], off
	v_mad_i64_i32 v[0:1], s[36:37], s36, v205, v[126:127]
	v_lshl_add_u64 v[2:3], v[0:1], 0, s[78:79]
	v_lshl_add_u64 v[0:1], v[0:1], 0, s[20:21]
	s_add_i32 s35, s62, s35
	global_load_dword v66, v[2:3], off
	global_load_dword v57, v[0:1], off
	v_mad_i64_i32 v[0:1], s[36:37], s35, v205, v[126:127]
	v_lshl_add_u64 v[2:3], v[0:1], 0, s[78:79]
	v_lshl_add_u64 v[0:1], v[0:1], 0, s[20:21]
	s_add_i32 s34, s62, s34
	global_load_dword v71, v[2:3], off
	global_load_dword v58, v[0:1], off
	v_mad_i64_i32 v[0:1], s[34:35], s34, v205, v[126:127]
	v_lshl_add_u64 v[2:3], v[0:1], 0, s[78:79]
	v_lshl_add_u64 v[0:1], v[0:1], 0, s[20:21]
	s_add_i32 s27, s62, s27
	global_load_dword v72, v[2:3], off
	global_load_dword v60, v[0:1], off
	v_mad_i64_i32 v[0:1], s[34:35], s27, v205, v[126:127]
	v_lshl_add_u64 v[2:3], v[0:1], 0, s[78:79]
	v_lshl_add_u64 v[0:1], v[0:1], 0, s[20:21]
	s_add_i32 s62, s62, s26
	global_load_dword v73, v[2:3], off
	global_load_dword v62, v[0:1], off
	v_mad_i64_i32 v[0:1], s[26:27], s62, v205, v[126:127]
	v_lshl_add_u64 v[2:3], v[0:1], 0, s[78:79]
	v_lshl_add_u64 v[0:1], v[0:1], 0, s[20:21]
	global_load_dword v76, v[2:3], off
	global_load_dword v70, v[0:1], off
	s_waitcnt lgkmcnt(0)
	s_barrier
	ds_read_b128 v[0:3], v170 offset:32768
	ds_read_b128 v[30:33], v170 offset:33792
	ds_read_b128 v[244:247], v160 offset:49152
	ds_read_b128 v[248:251], v160 offset:50176
	ds_read_b128 v[252:255], v160 offset:51200
	ds_read_b128 v[196:199], v160 offset:52224
	s_waitcnt lgkmcnt(3)
	v_mfma_f32_16x16x32_bf16 v[34:37], v[0:3], v[244:247], 0
	s_waitcnt vmcnt(47)
	v_lshlrev_b32_e32 v14, 16, v16
	v_and_b32_e32 v16, 0xffff0000, v16
	v_mul_f32_e32 v14, v46, v14
	s_waitcnt lgkmcnt(2)
	v_mfma_f32_16x16x32_bf16 v[34:37], v[30:33], v[248:251], v[34:37]
	ds_read_b128 v[244:247], v160 offset:53248
	ds_read_b128 v[248:251], v160 offset:54272
	v_mul_f32_e32 v16, v46, v16
	s_waitcnt vmcnt(41)
	v_and_b32_e32 v21, 0xffff0000, v22
	v_mul_f32_e32 v21, v49, v21
	s_add_i32 s20, s24, s25
	s_ashr_i32 s21, s20, 31
	s_nop 1
	v_pk_fma_f32 v[38:39], v[8:9], 0, v[34:35] op_sel_hi:[0,0,1]
	v_pk_fma_f32 v[42:43], v[8:9], 0, v[36:37] op_sel_hi:[0,0,1]
	s_waitcnt lgkmcnt(3)
	v_mfma_f32_16x16x32_bf16 v[34:37], v[0:3], v[252:255], 0
	s_lshl_b64 s[26:27], s[20:21], 15
	v_readlane_b32 s34, v242, 58
	s_add_u32 s26, s34, s26
	s_waitcnt lgkmcnt(2)
	v_mfma_f32_16x16x32_bf16 v[34:37], v[30:33], v[196:199], v[34:37]
	ds_read_b128 v[252:255], v160 offset:55296
	ds_read_b128 v[196:199], v160 offset:56320
	v_readlane_b32 s34, v242, 60
	s_addc_u32 s27, s34, s27
	s_mov_b64 s[34:35], 0
	s_and_b64 vcc, exec, s[28:29]
	s_nop 3
	v_pk_fma_f32 v[88:89], v[8:9], 0, v[34:35] op_sel_hi:[0,0,1]
	v_pk_fma_f32 v[90:91], v[8:9], 0, v[36:37] op_sel_hi:[0,0,1]
	s_waitcnt lgkmcnt(3)
	v_mfma_f32_16x16x32_bf16 v[34:37], v[0:3], v[244:247], 0
	s_waitcnt lgkmcnt(2)
	v_mfma_f32_16x16x32_bf16 v[34:37], v[30:33], v[248:251], v[34:37]
	ds_read_b128 v[244:247], v160 offset:57344
	ds_read_b128 v[248:251], v160 offset:58368
	s_nop 7
	v_pk_fma_f32 v[92:93], v[8:9], 0, v[34:35] op_sel_hi:[0,0,1]
	v_pk_fma_f32 v[94:95], v[8:9], 0, v[36:37] op_sel_hi:[0,0,1]
	s_waitcnt lgkmcnt(3)
	v_mfma_f32_16x16x32_bf16 v[34:37], v[0:3], v[252:255], 0
	s_waitcnt lgkmcnt(2)
	v_mfma_f32_16x16x32_bf16 v[34:37], v[30:33], v[196:199], v[34:37]
	ds_read_b128 v[252:255], v160 offset:59392
	ds_read_b128 v[196:199], v160 offset:60416
	s_nop 7
	v_pk_fma_f32 v[96:97], v[8:9], 0, v[34:35] op_sel_hi:[0,0,1]
	v_pk_fma_f32 v[98:99], v[8:9], 0, v[36:37] op_sel_hi:[0,0,1]
	s_waitcnt lgkmcnt(3)
	v_mfma_f32_16x16x32_bf16 v[34:37], v[0:3], v[244:247], 0
	s_waitcnt lgkmcnt(2)
	v_mfma_f32_16x16x32_bf16 v[34:37], v[30:33], v[248:251], v[34:37]
	ds_read_b128 v[244:247], v160 offset:61440
	ds_read_b128 v[248:251], v160 offset:62464
	s_nop 7
	v_pk_fma_f32 v[100:101], v[8:9], 0, v[34:35] op_sel_hi:[0,0,1]
	v_pk_fma_f32 v[102:103], v[8:9], 0, v[36:37] op_sel_hi:[0,0,1]
	s_waitcnt lgkmcnt(3)
	v_mfma_f32_16x16x32_bf16 v[34:37], v[0:3], v[252:255], 0
	s_waitcnt lgkmcnt(2)
	v_mfma_f32_16x16x32_bf16 v[34:37], v[30:33], v[196:199], v[34:37]
	ds_read_b128 v[252:255], v160 offset:63488
	ds_read_b128 v[196:199], v160 offset:64512
	s_nop 7
	v_pk_fma_f32 v[104:105], v[8:9], 0, v[34:35] op_sel_hi:[0,0,1]
	v_pk_fma_f32 v[106:107], v[8:9], 0, v[36:37] op_sel_hi:[0,0,1]
	s_waitcnt lgkmcnt(3)
	v_mfma_f32_16x16x32_bf16 v[34:37], v[0:3], v[244:247], 0
	s_waitcnt lgkmcnt(2)
	v_mfma_f32_16x16x32_bf16 v[34:37], v[30:33], v[248:251], v[34:37]
	s_nop 7
	v_pk_fma_f32 v[108:109], v[8:9], 0, v[34:35] op_sel_hi:[0,0,1]
	v_pk_fma_f32 v[110:111], v[8:9], 0, v[36:37] op_sel_hi:[0,0,1]
	v_cvt_pk_bf16_f32 v14, v14, v16
	v_lshlrev_b32_e32 v16, 16, v18
	v_and_b32_e32 v18, 0xffff0000, v18
	v_mul_f32_e32 v16, v47, v16
	v_mul_f32_e32 v18, v47, v18
	v_cvt_pk_bf16_f32 v16, v16, v18
	v_lshlrev_b32_e32 v18, 16, v20
	v_and_b32_e32 v20, 0xffff0000, v20
	v_mul_f32_e32 v18, v48, v18
	v_mul_f32_e32 v20, v48, v20
	v_cvt_pk_bf16_f32 v18, v18, v20
	v_lshlrev_b32_e32 v20, 16, v22
	v_mul_f32_e32 v20, v49, v20
	s_waitcnt lgkmcnt(1)
	v_mfma_f32_16x16x32_bf16 v[0:3], v[0:3], v[252:255], 0
	v_cvt_pk_bf16_f32 v28, v20, v21
	s_waitcnt vmcnt(39)
	v_lshlrev_b32_e32 v20, 16, v25
	v_mul_f32_e32 v20, v50, v20
	v_and_b32_e32 v21, 0xffff0000, v25
	v_mul_f32_e32 v21, v50, v21
	v_cvt_pk_bf16_f32 v25, v20, v21
	s_waitcnt vmcnt(37)
	v_lshlrev_b32_e32 v20, 16, v26
	v_mul_f32_e32 v20, v51, v20
	v_and_b32_e32 v21, 0xffff0000, v26
	s_waitcnt lgkmcnt(0)
	v_mfma_f32_16x16x32_bf16 v[0:3], v[30:33], v[196:199], v[0:3]
	v_mul_f32_e32 v21, v51, v21
	v_cvt_pk_bf16_f32 v30, v20, v21
	s_waitcnt vmcnt(35)
	v_lshlrev_b32_e32 v20, 16, v27
	v_mul_f32_e32 v20, v52, v20
	v_and_b32_e32 v21, 0xffff0000, v27
	v_mul_f32_e32 v21, v52, v21
	v_cvt_pk_bf16_f32 v31, v20, v21
	s_waitcnt vmcnt(33)
	v_lshlrev_b32_e32 v20, 16, v29
	v_mul_f32_e32 v20, v53, v20
	v_and_b32_e32 v21, 0xffff0000, v29
	v_mul_f32_e32 v21, v53, v21
	v_cvt_pk_bf16_f32 v29, v20, v21
	v_and_b32_e32 v20, 0xffff, v14
	v_lshrrev_b32_e32 v14, 16, v14
	v_and_or_b32 v26, v16, s95, v14
	v_lshrrev_b32_e32 v14, 16, v18
	v_and_b32_e32 v21, 0xffff, v18
	v_and_or_b32 v27, v28, s95, v14
	v_lshrrev_b32_e32 v14, 16, v25
	v_lshl_or_b32 v21, v28, 16, v21
	v_and_b32_e32 v22, 0xffff, v25
	v_and_b32_e32 v23, 0xffff, v31
	v_and_or_b32 v28, v30, s95, v14
	v_lshrrev_b32_e32 v14, 16, v31
	v_lshl_or_b32 v20, v16, 16, v20
	v_lshl_or_b32 v22, v30, 16, v22
	v_lshl_or_b32 v23, v29, 16, v23
	v_and_or_b32 v29, v29, s95, v14
	v_and_b32_e32 v14, 0xffff, v10
	ds_write_b128 v161, v[20:23]
	ds_write_b128 v161, v[26:29] offset:64
	v_lshl_or_b32 v20, v11, 16, v14
	v_and_b32_e32 v14, 0xffff, v12
	v_lshl_or_b32 v21, v13, 16, v14
	v_and_b32_e32 v14, 0xffff, v15
	v_lshrrev_b32_e32 v10, 16, v10
	v_lshl_or_b32 v22, v17, 16, v14
	v_and_b32_e32 v14, 0xffff, v19
	v_and_or_b32 v10, v11, s95, v10
	v_lshrrev_b32_e32 v11, 16, v12
	s_waitcnt vmcnt(32)
	v_lshl_or_b32 v23, v24, 16, v14
	v_and_or_b32 v11, v13, s95, v11
	v_lshrrev_b32_e32 v12, 16, v15
	v_lshrrev_b32_e32 v13, 16, v19
	v_and_or_b32 v12, v17, s95, v12
	v_and_or_b32 v13, v24, s95, v13
	ds_write_b128 v161, v[20:23] offset:16384
	ds_write_b128 v161, v[10:13] offset:16448
	s_waitcnt lgkmcnt(0)
	s_barrier
	ds_read_b128 v[80:83], v170
	ds_read_b128 v[84:87], v170 offset:1024
	ds_read_b128 v[244:247], v160 offset:16384
	ds_read_b128 v[248:251], v160 offset:17408
	ds_read_b128 v[252:255], v160 offset:18432
	ds_read_b128 v[196:199], v160 offset:19456
	s_waitcnt lgkmcnt(3)
	v_mfma_f32_16x16x32_bf16 v[10:13], v[80:83], v[244:247], 0
	v_fma_f32 v0, v8, 0, v0
	v_fma_f32 v1, v8, 0, v1
	v_pk_fma_f32 v[2:3], v[8:9], 0, v[2:3] op_sel_hi:[0,0,1]
	s_waitcnt lgkmcnt(2)
	v_mfma_f32_16x16x32_bf16 v[10:13], v[84:87], v[248:251], v[10:13]
	ds_read_b128 v[244:247], v160 offset:20480
	ds_read_b128 v[248:251], v160 offset:21504
	s_nop 7
	v_pk_fma_f32 v[26:27], v[8:9], v[42:43], v[12:13] op_sel_hi:[0,1,1]
	v_pk_fma_f32 v[14:15], v[8:9], v[38:39], v[10:11] op_sel_hi:[0,1,1]
	s_waitcnt lgkmcnt(3)
	v_mfma_f32_16x16x32_bf16 v[10:13], v[80:83], v[252:255], 0
	s_waitcnt lgkmcnt(2)
	v_mfma_f32_16x16x32_bf16 v[10:13], v[84:87], v[196:199], v[10:13]
	ds_read_b128 v[252:255], v160 offset:22528
	ds_read_b128 v[196:199], v160 offset:23552
	s_nop 7
	v_pk_fma_f32 v[28:29], v[8:9], v[90:91], v[12:13] op_sel_hi:[0,1,1]
	v_pk_fma_f32 v[16:17], v[8:9], v[88:89], v[10:11] op_sel_hi:[0,1,1]
	s_waitcnt lgkmcnt(3)
	v_mfma_f32_16x16x32_bf16 v[10:13], v[80:83], v[244:247], 0
	s_waitcnt lgkmcnt(2)
	v_mfma_f32_16x16x32_bf16 v[10:13], v[84:87], v[248:251], v[10:13]
	ds_read_b128 v[244:247], v160 offset:24576
	ds_read_b128 v[248:251], v160 offset:25600
	s_nop 7
	v_pk_fma_f32 v[30:31], v[8:9], v[94:95], v[12:13] op_sel_hi:[0,1,1]
	v_pk_fma_f32 v[18:19], v[8:9], v[92:93], v[10:11] op_sel_hi:[0,1,1]
	s_waitcnt lgkmcnt(3)
	v_mfma_f32_16x16x32_bf16 v[10:13], v[80:83], v[252:255], 0
	s_waitcnt lgkmcnt(2)
	v_mfma_f32_16x16x32_bf16 v[10:13], v[84:87], v[196:199], v[10:13]
	ds_read_b128 v[252:255], v160 offset:26624
	ds_read_b128 v[196:199], v160 offset:27648
	s_nop 7
	v_pk_fma_f32 v[32:33], v[8:9], v[98:99], v[12:13] op_sel_hi:[0,1,1]
	v_pk_fma_f32 v[20:21], v[8:9], v[96:97], v[10:11] op_sel_hi:[0,1,1]
	s_waitcnt lgkmcnt(3)
	v_mfma_f32_16x16x32_bf16 v[10:13], v[80:83], v[244:247], 0
	s_waitcnt lgkmcnt(2)
	v_mfma_f32_16x16x32_bf16 v[10:13], v[84:87], v[248:251], v[10:13]
	ds_read_b128 v[244:247], v160 offset:28672
	ds_read_b128 v[248:251], v160 offset:29696
	s_nop 7
	v_pk_fma_f32 v[34:35], v[8:9], v[102:103], v[12:13] op_sel_hi:[0,1,1]
	v_pk_fma_f32 v[22:23], v[8:9], v[100:101], v[10:11] op_sel_hi:[0,1,1]
	s_waitcnt lgkmcnt(3)
	v_mfma_f32_16x16x32_bf16 v[10:13], v[80:83], v[252:255], 0
	s_waitcnt lgkmcnt(2)
	v_mfma_f32_16x16x32_bf16 v[10:13], v[84:87], v[196:199], v[10:13]
	ds_read_b128 v[252:255], v160 offset:30720
	ds_read_b128 v[196:199], v160 offset:31744
	s_nop 7
	v_pk_fma_f32 v[36:37], v[8:9], v[106:107], v[12:13] op_sel_hi:[0,1,1]
	v_pk_fma_f32 v[24:25], v[8:9], v[104:105], v[10:11] op_sel_hi:[0,1,1]
	s_waitcnt lgkmcnt(3)
	v_mfma_f32_16x16x32_bf16 v[10:13], v[80:83], v[244:247], 0
	s_waitcnt lgkmcnt(2)
	v_mfma_f32_16x16x32_bf16 v[88:91], v[84:87], v[248:251], v[10:13]
	s_nop 7
	v_pk_fma_f32 v[10:11], v[8:9], v[110:111], v[90:91] op_sel_hi:[0,1,1]
	v_pk_fma_f32 v[12:13], v[8:9], v[108:109], v[88:89] op_sel_hi:[0,1,1]
	s_waitcnt lgkmcnt(1)
	v_mfma_f32_16x16x32_bf16 v[80:83], v[80:83], v[252:255], 0
	s_waitcnt lgkmcnt(0)
	v_mfma_f32_16x16x32_bf16 v[80:83], v[84:87], v[196:199], v[80:83]
	s_nop 7
	v_pk_fma_f32 v[42:43], v[8:9], v[0:1], v[80:81] op_sel_hi:[0,1,1]
	s_waitcnt vmcnt(31)
	v_lshlrev_b32_e32 v0, 16, v41
	v_mul_f32_e32 v0, v46, v0
	v_and_b32_e32 v1, 0xffff0000, v41
	v_mul_f32_e32 v1, v46, v1
	v_cvt_pk_bf16_f32 v41, v0, v1
	s_waitcnt vmcnt(29)
	v_lshlrev_b32_e32 v0, 16, v45
	v_mul_f32_e32 v0, v47, v0
	v_and_b32_e32 v1, 0xffff0000, v45
	v_mul_f32_e32 v1, v47, v1
	v_cvt_pk_bf16_f32 v45, v0, v1
	s_waitcnt vmcnt(27)
	v_lshlrev_b32_e32 v0, 16, v68
	v_mul_f32_e32 v0, v48, v0
	v_and_b32_e32 v1, 0xffff0000, v68
	v_mul_f32_e32 v1, v48, v1
	v_cvt_pk_bf16_f32 v68, v0, v1
	s_waitcnt vmcnt(25)
	v_lshlrev_b32_e32 v0, 16, v69
	v_mul_f32_e32 v0, v49, v0
	v_and_b32_e32 v1, 0xffff0000, v69
	v_mul_f32_e32 v1, v49, v1
	v_cvt_pk_bf16_f32 v69, v0, v1
	s_waitcnt vmcnt(23)
	v_lshlrev_b32_e32 v0, 16, v75
	v_mul_f32_e32 v0, v50, v0
	v_and_b32_e32 v1, 0xffff0000, v75
	v_mul_f32_e32 v1, v50, v1
	v_cvt_pk_bf16_f32 v75, v0, v1
	s_waitcnt vmcnt(21)
	v_lshlrev_b32_e32 v0, 16, v77
	v_mul_f32_e32 v0, v51, v0
	v_and_b32_e32 v1, 0xffff0000, v77
	v_mul_f32_e32 v1, v51, v1
	v_cvt_pk_bf16_f32 v77, v0, v1
	s_waitcnt vmcnt(19)
	v_lshlrev_b32_e32 v0, 16, v78
	v_mul_f32_e32 v0, v52, v0
	v_and_b32_e32 v1, 0xffff0000, v78
	v_mul_f32_e32 v1, v52, v1
	v_cvt_pk_bf16_f32 v81, v0, v1
	s_waitcnt vmcnt(17)
	v_lshlrev_b32_e32 v0, 16, v79
	v_mul_f32_e32 v0, v53, v0
	v_and_b32_e32 v1, 0xffff0000, v79
	v_pk_fma_f32 v[38:39], v[8:9], v[2:3], v[82:83] op_sel_hi:[0,1,1]
	v_mul_f32_e32 v1, v53, v1
	v_cvt_pk_bf16_f32 v82, v0, v1
	v_and_b32_e32 v0, 0xffff, v41
	v_lshrrev_b32_e32 v41, 16, v41
	v_and_or_b32 v78, v45, s95, v41
	v_lshrrev_b32_e32 v41, 16, v68
	v_and_b32_e32 v1, 0xffff, v68
	v_and_b32_e32 v2, 0xffff, v75
	v_and_b32_e32 v3, 0xffff, v81
	v_and_or_b32 v79, v69, s95, v41
	v_lshrrev_b32_e32 v41, 16, v75
	v_lshl_or_b32 v0, v45, 16, v0
	v_lshl_or_b32 v1, v69, 16, v1
	v_lshl_or_b32 v2, v77, 16, v2
	v_lshl_or_b32 v3, v82, 16, v3
	v_and_or_b32 v80, v77, s95, v41
	v_lshrrev_b32_e32 v41, 16, v81
	v_and_or_b32 v81, v82, s95, v41
	ds_write_b128 v161, v[0:3] offset:32768
	ds_write_b128 v161, v[78:81] offset:32832
	v_and_b32_e32 v0, 0xffff, v4
	v_lshrrev_b32_e32 v4, 16, v4
	v_lshl_or_b32 v0, v5, 16, v0
	v_and_b32_e32 v1, 0xffff, v6
	v_and_b32_e32 v2, 0xffff, v40
	v_and_b32_e32 v3, 0xffff, v67
	v_and_or_b32 v4, v5, s95, v4
	v_lshrrev_b32_e32 v5, 16, v6
	v_lshl_or_b32 v1, v7, 16, v1
	v_lshl_or_b32 v2, v44, 16, v2
	s_waitcnt vmcnt(16)
	v_lshl_or_b32 v3, v74, 16, v3
	v_and_or_b32 v5, v7, s95, v5
	v_lshrrev_b32_e32 v6, 16, v40
	v_lshrrev_b32_e32 v7, 16, v67
	v_and_or_b32 v6, v44, s95, v6
	v_and_or_b32 v7, v74, s95, v7
	ds_write_b128 v161, v[0:3] offset:49152
	ds_write_b128 v161, v[4:7] offset:49216
	s_waitcnt lgkmcnt(0)
	s_barrier
	ds_read_b128 v[0:3], v170 offset:32768
	ds_read_b128 v[4:7], v170 offset:33792
	ds_read_b128 v[244:247], v160 offset:49152
	ds_read_b128 v[248:251], v160 offset:50176
	ds_read_b128 v[252:255], v160 offset:51200
	ds_read_b128 v[196:199], v160 offset:52224
	s_waitcnt lgkmcnt(3)
	v_mfma_f32_16x16x32_bf16 v[78:81], v[0:3], v[244:247], 0
	s_waitcnt lgkmcnt(2)
	v_mfma_f32_16x16x32_bf16 v[78:81], v[4:7], v[248:251], v[78:81]
	ds_read_b128 v[244:247], v160 offset:53248
	ds_read_b128 v[248:251], v160 offset:54272
	s_nop 7
	v_pk_fma_f32 v[14:15], v[8:9], v[14:15], v[78:79] op_sel_hi:[0,1,1]
	v_pk_fma_f32 v[26:27], v[8:9], v[26:27], v[80:81] op_sel_hi:[0,1,1]
	s_waitcnt lgkmcnt(3)
	v_mfma_f32_16x16x32_bf16 v[78:81], v[0:3], v[252:255], 0
	s_waitcnt lgkmcnt(2)
	v_mfma_f32_16x16x32_bf16 v[78:81], v[4:7], v[196:199], v[78:81]
	ds_read_b128 v[252:255], v160 offset:55296
	ds_read_b128 v[196:199], v160 offset:56320
	s_nop 7
	v_pk_fma_f32 v[16:17], v[8:9], v[16:17], v[78:79] op_sel_hi:[0,1,1]
	v_pk_fma_f32 v[28:29], v[8:9], v[28:29], v[80:81] op_sel_hi:[0,1,1]
	s_waitcnt lgkmcnt(3)
	v_mfma_f32_16x16x32_bf16 v[78:81], v[0:3], v[244:247], 0
	s_waitcnt lgkmcnt(2)
	v_mfma_f32_16x16x32_bf16 v[78:81], v[4:7], v[248:251], v[78:81]
	ds_read_b128 v[244:247], v160 offset:57344
	ds_read_b128 v[248:251], v160 offset:58368
	s_nop 7
	v_pk_fma_f32 v[18:19], v[8:9], v[18:19], v[78:79] op_sel_hi:[0,1,1]
	v_pk_fma_f32 v[30:31], v[8:9], v[30:31], v[80:81] op_sel_hi:[0,1,1]
	s_waitcnt lgkmcnt(3)
	v_mfma_f32_16x16x32_bf16 v[78:81], v[0:3], v[252:255], 0
	s_waitcnt lgkmcnt(2)
	v_mfma_f32_16x16x32_bf16 v[78:81], v[4:7], v[196:199], v[78:81]
	ds_read_b128 v[252:255], v160 offset:59392
	ds_read_b128 v[196:199], v160 offset:60416
	s_nop 7
	v_pk_fma_f32 v[20:21], v[8:9], v[20:21], v[78:79] op_sel_hi:[0,1,1]
	v_pk_fma_f32 v[32:33], v[8:9], v[32:33], v[80:81] op_sel_hi:[0,1,1]
	s_waitcnt lgkmcnt(3)
	v_mfma_f32_16x16x32_bf16 v[78:81], v[0:3], v[244:247], 0
	s_waitcnt lgkmcnt(2)
	v_mfma_f32_16x16x32_bf16 v[78:81], v[4:7], v[248:251], v[78:81]
	ds_read_b128 v[244:247], v160 offset:61440
	ds_read_b128 v[248:251], v160 offset:62464
	s_nop 7
	v_pk_fma_f32 v[22:23], v[8:9], v[22:23], v[78:79] op_sel_hi:[0,1,1]
	v_pk_fma_f32 v[34:35], v[8:9], v[34:35], v[80:81] op_sel_hi:[0,1,1]
	s_waitcnt lgkmcnt(3)
	v_mfma_f32_16x16x32_bf16 v[78:81], v[0:3], v[252:255], 0
	s_waitcnt lgkmcnt(2)
	v_mfma_f32_16x16x32_bf16 v[78:81], v[4:7], v[196:199], v[78:81]
	ds_read_b128 v[252:255], v160 offset:63488
	ds_read_b128 v[196:199], v160 offset:64512
	s_nop 7
	v_pk_fma_f32 v[24:25], v[8:9], v[24:25], v[78:79] op_sel_hi:[0,1,1]
	v_pk_fma_f32 v[36:37], v[8:9], v[36:37], v[80:81] op_sel_hi:[0,1,1]
	s_waitcnt lgkmcnt(3)
	v_mfma_f32_16x16x32_bf16 v[78:81], v[0:3], v[244:247], 0
	s_waitcnt lgkmcnt(2)
	v_mfma_f32_16x16x32_bf16 v[78:81], v[4:7], v[248:251], v[78:81]
	s_nop 7
	v_pk_fma_f32 v[40:41], v[8:9], v[12:13], v[78:79] op_sel_hi:[0,1,1]
	v_pk_fma_f32 v[44:45], v[8:9], v[10:11], v[80:81] op_sel_hi:[0,1,1]
	s_waitcnt lgkmcnt(1)
	v_mfma_f32_16x16x32_bf16 v[0:3], v[0:3], v[252:255], 0
	s_waitcnt lgkmcnt(0)
	v_mfma_f32_16x16x32_bf16 v[0:3], v[4:7], v[196:199], v[0:3]
	s_nop 7
	v_pk_fma_f32 v[10:11], v[8:9], v[42:43], v[0:1] op_sel_hi:[0,1,1]
	s_waitcnt vmcnt(15)
	v_lshlrev_b32_e32 v0, 16, v59
	v_mul_f32_e32 v0, v46, v0
	v_and_b32_e32 v1, 0xffff0000, v59
	v_mul_f32_e32 v1, v46, v1
	v_cvt_pk_bf16_f32 v4, v0, v1
	s_waitcnt vmcnt(13)
	v_lshlrev_b32_e32 v0, 16, v61
	v_mul_f32_e32 v0, v47, v0
	v_and_b32_e32 v1, 0xffff0000, v61
	v_mul_f32_e32 v1, v47, v1
	v_cvt_pk_bf16_f32 v5, v0, v1
	s_waitcnt vmcnt(11)
	v_lshlrev_b32_e32 v0, 16, v63
	v_mul_f32_e32 v0, v48, v0
	v_and_b32_e32 v1, 0xffff0000, v63
	v_mul_f32_e32 v1, v48, v1
	v_cvt_pk_bf16_f32 v6, v0, v1
	s_waitcnt vmcnt(9)
	v_lshlrev_b32_e32 v0, 16, v66
	v_mul_f32_e32 v0, v49, v0
	v_and_b32_e32 v1, 0xffff0000, v66
	v_mul_f32_e32 v1, v49, v1
	v_cvt_pk_bf16_f32 v7, v0, v1
	s_waitcnt vmcnt(7)
	v_lshlrev_b32_e32 v0, 16, v71
	v_mul_f32_e32 v0, v50, v0
	v_and_b32_e32 v1, 0xffff0000, v71
	v_pk_fma_f32 v[12:13], v[8:9], v[38:39], v[2:3] op_sel_hi:[0,1,1]
	v_mul_f32_e32 v1, v50, v1
	v_cvt_pk_bf16_f32 v38, v0, v1
	s_waitcnt vmcnt(5)
	v_lshlrev_b32_e32 v0, 16, v72
	v_mul_f32_e32 v0, v51, v0
	v_and_b32_e32 v1, 0xffff0000, v72
	v_mul_f32_e32 v1, v51, v1
	v_cvt_pk_bf16_f32 v39, v0, v1
	s_waitcnt vmcnt(3)
	v_lshlrev_b32_e32 v0, 16, v73
	v_mul_f32_e32 v0, v52, v0
	v_and_b32_e32 v1, 0xffff0000, v73
	v_mul_f32_e32 v1, v52, v1
	v_cvt_pk_bf16_f32 v42, v0, v1
	s_waitcnt vmcnt(1)
	v_lshlrev_b32_e32 v0, 16, v76
	v_mul_f32_e32 v0, v53, v0
	v_and_b32_e32 v1, 0xffff0000, v76
	v_mul_f32_e32 v1, v53, v1
	v_cvt_pk_bf16_f32 v43, v0, v1
	v_and_b32_e32 v0, 0xffff, v4
	v_lshrrev_b32_e32 v4, 16, v4
	v_lshl_or_b32 v0, v5, 16, v0
	v_and_b32_e32 v1, 0xffff, v6
	v_and_b32_e32 v2, 0xffff, v38
	v_and_b32_e32 v3, 0xffff, v42
	v_and_or_b32 v4, v5, s95, v4
	v_lshrrev_b32_e32 v5, 16, v6
	v_lshl_or_b32 v1, v7, 16, v1
	v_lshl_or_b32 v2, v39, 16, v2
	v_lshl_or_b32 v3, v43, 16, v3
	v_and_or_b32 v5, v7, s95, v5
	v_lshrrev_b32_e32 v6, 16, v38
	v_lshrrev_b32_e32 v7, 16, v42
	v_and_or_b32 v6, v39, s95, v6
	v_and_or_b32 v7, v43, s95, v7
	ds_write_b128 v161, v[0:3]
	ds_write_b128 v161, v[4:7] offset:64
	v_and_b32_e32 v0, 0xffff, v54
	v_and_b32_e32 v1, 0xffff, v56
	v_and_b32_e32 v2, 0xffff, v58
	v_and_b32_e32 v3, 0xffff, v62
	v_lshl_or_b32 v0, v55, 16, v0
	v_lshl_or_b32 v1, v57, 16, v1
	v_lshl_or_b32 v2, v60, 16, v2
	s_waitcnt vmcnt(0)
	v_lshl_or_b32 v3, v70, 16, v3
	v_lshrrev_b32_e32 v4, 16, v54
	v_lshrrev_b32_e32 v5, 16, v56
	v_lshrrev_b32_e32 v6, 16, v58
	v_lshrrev_b32_e32 v7, 16, v62
	v_and_or_b32 v4, v55, s95, v4
	v_and_or_b32 v5, v57, s95, v5
	v_and_or_b32 v6, v60, s95, v6
	v_and_or_b32 v7, v70, s95, v7
	ds_write_b128 v161, v[0:3] offset:16384
	ds_write_b128 v161, v[4:7] offset:16448
	s_waitcnt lgkmcnt(0)
	s_barrier
	ds_read_b128 v[4:7], v170
	ds_read_b128 v[0:3], v170 offset:1024
	ds_read_b128 v[244:247], v160 offset:16384
	ds_read_b128 v[248:251], v160 offset:17408
	ds_read_b128 v[252:255], v160 offset:18432
	ds_read_b128 v[196:199], v160 offset:19456
	s_waitcnt lgkmcnt(3)
	v_mfma_f32_16x16x32_bf16 v[46:49], v[4:7], v[244:247], 0
	s_waitcnt lgkmcnt(2)
	v_mfma_f32_16x16x32_bf16 v[46:49], v[0:3], v[248:251], v[46:49]
	ds_read_b128 v[244:247], v160 offset:20480
	ds_read_b128 v[248:251], v160 offset:21504
	s_nop 7
	v_pk_fma_f32 v[26:27], v[8:9], v[26:27], v[48:49] op_sel_hi:[0,1,1]
	v_pk_fma_f32 v[14:15], v[8:9], v[14:15], v[46:47] op_sel_hi:[0,1,1]
	s_waitcnt lgkmcnt(3)
	v_mfma_f32_16x16x32_bf16 v[46:49], v[4:7], v[252:255], 0
	s_waitcnt lgkmcnt(2)
	v_mfma_f32_16x16x32_bf16 v[46:49], v[0:3], v[196:199], v[46:49]
	ds_read_b128 v[252:255], v160 offset:22528
	ds_read_b128 v[196:199], v160 offset:23552
	s_nop 7
	v_pk_fma_f32 v[28:29], v[8:9], v[28:29], v[48:49] op_sel_hi:[0,1,1]
	v_pk_fma_f32 v[16:17], v[8:9], v[16:17], v[46:47] op_sel_hi:[0,1,1]
	s_waitcnt lgkmcnt(3)
	v_mfma_f32_16x16x32_bf16 v[46:49], v[4:7], v[244:247], 0
	s_waitcnt lgkmcnt(2)
	v_mfma_f32_16x16x32_bf16 v[46:49], v[0:3], v[248:251], v[46:49]
	ds_read_b128 v[244:247], v160 offset:24576
	ds_read_b128 v[248:251], v160 offset:25600
	s_nop 7
	v_pk_fma_f32 v[38:39], v[8:9], v[30:31], v[48:49] op_sel_hi:[0,1,1]
	v_pk_fma_f32 v[42:43], v[8:9], v[18:19], v[46:47] op_sel_hi:[0,1,1]
	s_waitcnt lgkmcnt(3)
	v_mfma_f32_16x16x32_bf16 v[46:49], v[4:7], v[252:255], 0
	s_waitcnt lgkmcnt(2)
	v_mfma_f32_16x16x32_bf16 v[46:49], v[0:3], v[196:199], v[46:49]
	ds_read_b128 v[252:255], v160 offset:26624
	ds_read_b128 v[196:199], v160 offset:27648
	s_nop 7
	v_pk_fma_f32 v[48:49], v[8:9], v[32:33], v[48:49] op_sel_hi:[0,1,1]
	v_pk_fma_f32 v[46:47], v[8:9], v[20:21], v[46:47] op_sel_hi:[0,1,1]
	s_waitcnt lgkmcnt(3)
	v_mfma_f32_16x16x32_bf16 v[18:21], v[4:7], v[244:247], 0
	s_waitcnt lgkmcnt(2)
	v_mfma_f32_16x16x32_bf16 v[18:21], v[0:3], v[248:251], v[18:21]
	ds_read_b128 v[244:247], v160 offset:28672
	ds_read_b128 v[248:251], v160 offset:29696
	s_nop 7
	v_pk_fma_f32 v[34:35], v[8:9], v[34:35], v[20:21] op_sel_hi:[0,1,1]
	v_pk_fma_f32 v[50:51], v[8:9], v[22:23], v[18:19] op_sel_hi:[0,1,1]
	s_waitcnt lgkmcnt(3)
	v_mfma_f32_16x16x32_bf16 v[18:21], v[4:7], v[252:255], 0
	s_waitcnt lgkmcnt(2)
	v_mfma_f32_16x16x32_bf16 v[18:21], v[0:3], v[196:199], v[18:21]
	ds_read_b128 v[252:255], v160 offset:30720
	ds_read_b128 v[196:199], v160 offset:31744
	s_nop 7
	v_pk_fma_f32 v[30:31], v[8:9], v[36:37], v[20:21] op_sel_hi:[0,1,1]
	v_pk_fma_f32 v[32:33], v[8:9], v[24:25], v[18:19] op_sel_hi:[0,1,1]
	s_waitcnt lgkmcnt(3)
	v_mfma_f32_16x16x32_bf16 v[18:21], v[4:7], v[244:247], 0
	s_waitcnt lgkmcnt(2)
	v_mfma_f32_16x16x32_bf16 v[18:21], v[0:3], v[248:251], v[18:21]
	s_nop 7
	v_pk_fma_f32 v[36:37], v[8:9], v[44:45], v[20:21] op_sel_hi:[0,1,1]
	v_pk_fma_f32 v[40:41], v[8:9], v[40:41], v[18:19] op_sel_hi:[0,1,1]
	s_waitcnt lgkmcnt(1)
	v_mfma_f32_16x16x32_bf16 v[4:7], v[4:7], v[252:255], 0
	s_waitcnt lgkmcnt(0)
	v_mfma_f32_16x16x32_bf16 v[0:3], v[0:3], v[196:199], v[4:7]
	v_cvt_pk_bf16_f32 v4, v14, v15
	v_cvt_pk_bf16_f32 v5, v26, v27
	s_nop 5
	v_lshl_add_u64 v[6:7], s[26:27], 0, v[122:123]
	global_store_dwordx2 v[6:7], v[4:5], off
	v_lshl_add_u64 v[6:7], s[26:27], 0, v[128:129]
	v_cvt_pk_bf16_f32 v4, v16, v17
	v_cvt_pk_bf16_f32 v5, v28, v29
	global_store_dwordx2 v[6:7], v[4:5], off
	v_lshl_add_u64 v[6:7], s[26:27], 0, v[130:131]
	v_cvt_pk_bf16_f32 v4, v42, v43
	v_cvt_pk_bf16_f32 v5, v38, v39
	global_store_dwordx2 v[6:7], v[4:5], off
	v_lshl_add_u64 v[6:7], s[26:27], 0, v[132:133]
	v_cvt_pk_bf16_f32 v4, v46, v47
	v_cvt_pk_bf16_f32 v5, v48, v49
	global_store_dwordx2 v[6:7], v[4:5], off
	v_lshl_add_u64 v[6:7], s[26:27], 0, v[134:135]
	v_cvt_pk_bf16_f32 v4, v50, v51
	v_cvt_pk_bf16_f32 v5, v34, v35
	global_store_dwordx2 v[6:7], v[4:5], off
	v_lshl_add_u64 v[6:7], s[26:27], 0, v[136:137]
	v_pk_fma_f32 v[2:3], v[8:9], v[12:13], v[2:3] op_sel_hi:[0,1,1]
	v_pk_fma_f32 v[0:1], v[8:9], v[10:11], v[0:1] op_sel_hi:[0,1,1]
	v_cvt_pk_bf16_f32 v4, v32, v33
	v_cvt_pk_bf16_f32 v5, v30, v31
	global_store_dwordx2 v[6:7], v[4:5], off
	v_lshl_add_u64 v[6:7], s[26:27], 0, v[138:139]
	v_cvt_pk_bf16_f32 v4, v40, v41
	v_cvt_pk_bf16_f32 v5, v36, v37
	global_store_dwordx2 v[6:7], v[4:5], off
	v_cvt_pk_bf16_f32 v0, v0, v1
	v_cvt_pk_bf16_f32 v1, v2, v3
	v_lshl_add_u64 v[2:3], s[26:27], 0, v[140:141]
	s_mov_b64 s[26:27], 0
	global_store_dwordx2 v[2:3], v[0:1], off
	s_cbranch_vccz .LBB0_561
	v_mul_f32_e32 v0, 0xc3800000, v9
	v_mul_f32_e32 v0, 0x3fb8aa3b, v0
	v_exp_f32_e32 v0, v0
	s_mov_b64 s[26:27], -1
	v_mov_b32_e32 v1, v0
	s_branch .LBB0_561

.LBB0_985:
	ds_read_b128 v[172:175], v133
	ds_read_b128 v[176:179], v133 offset:32768
	ds_read_b128 v[222:225], v133 offset:1024
	ds_read_b128 v[226:229], v133 offset:33792
	ds_read_b128 v[230:233], v133 offset:2048
	ds_read_b128 v[234:237], v133 offset:34816
	v_mov_b32_e32 v64, v65
	s_waitcnt vmcnt(30)
	v_dot2c_f32_bf16_e32 v64, v126, v126
	v_dot2c_f32_bf16_e32 v64, v127, v127
	s_waitcnt lgkmcnt(5)
	v_mfma_f32_16x16x32_bf16 v[172:175], v[172:175], v[126:129], 0
	v_dot2c_f32_bf16_e32 v64, v128, v128
	v_dot2c_f32_bf16_e32 v64, v129, v129
	v_dot2c_f32_bf16_e32 v64, v122, v122
	s_waitcnt lgkmcnt(4)
	v_mfma_f32_16x16x32_bf16 v[172:175], v[176:179], v[126:129], v[172:175]
	ds_read_b128 v[176:179], v133 offset:3072
	ds_read_b128 v[180:183], v133 offset:35840
	v_dot2c_f32_bf16_e32 v64, v123, v123
	v_dot2c_f32_bf16_e32 v64, v124, v124
	s_waitcnt lgkmcnt(5)
	v_mfma_f32_16x16x32_bf16 v[172:175], v[222:225], v[122:125], v[172:175]
	v_dot2c_f32_bf16_e32 v64, v125, v125
	s_waitcnt vmcnt(28)
	v_dot2c_f32_bf16_e32 v64, v118, v118
	v_dot2c_f32_bf16_e32 v64, v119, v119
	s_waitcnt lgkmcnt(4)
	v_mfma_f32_16x16x32_bf16 v[172:175], v[226:229], v[122:125], v[172:175]
	ds_read_b128 v[222:225], v133 offset:4096
	ds_read_b128 v[226:229], v133 offset:36864
	v_dot2c_f32_bf16_e32 v64, v120, v120
	v_dot2c_f32_bf16_e32 v64, v121, v121
	s_waitcnt lgkmcnt(5)
	v_mfma_f32_16x16x32_bf16 v[172:175], v[230:233], v[118:121], v[172:175]
	v_dot2c_f32_bf16_e32 v64, v114, v114
	v_dot2c_f32_bf16_e32 v64, v115, v115
	v_dot2c_f32_bf16_e32 v64, v116, v116
	s_waitcnt lgkmcnt(4)
	v_mfma_f32_16x16x32_bf16 v[172:175], v[234:237], v[118:121], v[172:175]
	ds_read_b128 v[230:233], v133 offset:5120
	ds_read_b128 v[234:237], v133 offset:37888
	v_lshlrev_b64 v[144:145], 10, v[142:143]
	v_dot2c_f32_bf16_e32 v64, v117, v117
	s_waitcnt lgkmcnt(5)
	v_mfma_f32_16x16x32_bf16 v[172:175], v[176:179], v[114:117], v[172:175]
	s_waitcnt lgkmcnt(4)
	v_mfma_f32_16x16x32_bf16 v[172:175], v[180:183], v[114:117], v[172:175]
	ds_read_b128 v[176:179], v133 offset:6144
	ds_read_b128 v[180:183], v133 offset:38912
	s_waitcnt vmcnt(26)
	v_dot2c_f32_bf16_e32 v64, v110, v110
	v_dot2c_f32_bf16_e32 v64, v111, v111
	v_dot2c_f32_bf16_e32 v64, v112, v112
	s_waitcnt lgkmcnt(5)
	v_mfma_f32_16x16x32_bf16 v[172:175], v[222:225], v[110:113], v[172:175]
	v_dot2c_f32_bf16_e32 v64, v113, v113
	v_dot2c_f32_bf16_e32 v64, v106, v106
	v_dot2c_f32_bf16_e32 v64, v107, v107
	s_waitcnt lgkmcnt(4)
	v_mfma_f32_16x16x32_bf16 v[172:175], v[226:229], v[110:113], v[172:175]
	ds_read_b128 v[222:225], v133 offset:7168
	ds_read_b128 v[226:229], v133 offset:39936
	v_dot2c_f32_bf16_e32 v64, v108, v108
	v_dot2c_f32_bf16_e32 v64, v109, v109
	s_waitcnt lgkmcnt(5)
	v_mfma_f32_16x16x32_bf16 v[172:175], v[230:233], v[106:109], v[172:175]
	s_waitcnt vmcnt(24)
	v_dot2c_f32_bf16_e32 v64, v102, v102
	v_dot2c_f32_bf16_e32 v64, v103, v103
	v_dot2c_f32_bf16_e32 v64, v104, v104
	s_waitcnt lgkmcnt(4)
	v_mfma_f32_16x16x32_bf16 v[172:175], v[234:237], v[106:109], v[172:175]
	ds_read_b128 v[230:233], v133 offset:8192
	ds_read_b128 v[234:237], v133 offset:40960
	v_dot2c_f32_bf16_e32 v64, v105, v105
	v_dot2c_f32_bf16_e32 v64, v98, v98
	s_waitcnt lgkmcnt(5)
	v_mfma_f32_16x16x32_bf16 v[172:175], v[176:179], v[102:105], v[172:175]
	v_dot2c_f32_bf16_e32 v64, v99, v99
	v_dot2c_f32_bf16_e32 v64, v100, v100
	v_dot2c_f32_bf16_e32 v64, v101, v101
	s_waitcnt lgkmcnt(4)
	v_mfma_f32_16x16x32_bf16 v[172:175], v[180:183], v[102:105], v[172:175]
	ds_read_b128 v[176:179], v133 offset:9216
	ds_read_b128 v[180:183], v133 offset:41984
	s_waitcnt lgkmcnt(5)
	v_mfma_f32_16x16x32_bf16 v[172:175], v[222:225], v[98:101], v[172:175]
	s_waitcnt lgkmcnt(4)
	v_mfma_f32_16x16x32_bf16 v[172:175], v[226:229], v[98:101], v[172:175]
	ds_read_b128 v[222:225], v133 offset:10240
	ds_read_b128 v[226:229], v133 offset:43008
	s_waitcnt vmcnt(22)
	v_dot2c_f32_bf16_e32 v64, v94, v94
	v_dot2c_f32_bf16_e32 v64, v95, v95
	v_dot2c_f32_bf16_e32 v64, v96, v96
	s_waitcnt lgkmcnt(5)
	v_mfma_f32_16x16x32_bf16 v[172:175], v[230:233], v[94:97], v[172:175]
	v_dot2c_f32_bf16_e32 v64, v97, v97
	v_dot2c_f32_bf16_e32 v64, v90, v90
	v_dot2c_f32_bf16_e32 v64, v91, v91
	s_waitcnt lgkmcnt(4)
	v_mfma_f32_16x16x32_bf16 v[172:175], v[234:237], v[94:97], v[172:175]
	ds_read_b128 v[230:233], v133 offset:11264
	ds_read_b128 v[234:237], v133 offset:44032
	v_dot2c_f32_bf16_e32 v64, v92, v92
	v_dot2c_f32_bf16_e32 v64, v93, v93
	s_waitcnt lgkmcnt(5)
	v_mfma_f32_16x16x32_bf16 v[172:175], v[176:179], v[90:93], v[172:175]
	s_waitcnt vmcnt(20)
	v_dot2c_f32_bf16_e32 v64, v86, v86
	v_dot2c_f32_bf16_e32 v64, v87, v87
	v_dot2c_f32_bf16_e32 v64, v88, v88
	s_waitcnt lgkmcnt(4)
	v_mfma_f32_16x16x32_bf16 v[172:175], v[180:183], v[90:93], v[172:175]
	ds_read_b128 v[176:179], v133 offset:12288
	ds_read_b128 v[180:183], v133 offset:45056
	v_dot2c_f32_bf16_e32 v64, v89, v89
	v_dot2c_f32_bf16_e32 v64, v82, v82
	s_waitcnt lgkmcnt(5)
	v_mfma_f32_16x16x32_bf16 v[172:175], v[222:225], v[86:89], v[172:175]
	v_dot2c_f32_bf16_e32 v64, v83, v83
	v_dot2c_f32_bf16_e32 v64, v84, v84
	v_dot2c_f32_bf16_e32 v64, v85, v85
	s_waitcnt lgkmcnt(4)
	v_mfma_f32_16x16x32_bf16 v[172:175], v[226:229], v[86:89], v[172:175]
	ds_read_b128 v[222:225], v133 offset:13312
	ds_read_b128 v[226:229], v133 offset:46080
	s_waitcnt lgkmcnt(5)
	v_mfma_f32_16x16x32_bf16 v[172:175], v[230:233], v[82:85], v[172:175]
	s_waitcnt lgkmcnt(4)
	v_mfma_f32_16x16x32_bf16 v[172:175], v[234:237], v[82:85], v[172:175]
	ds_read_b128 v[230:233], v133 offset:14336
	ds_read_b128 v[234:237], v133 offset:47104
	s_waitcnt vmcnt(18)
	v_dot2c_f32_bf16_e32 v64, v78, v78
	v_dot2c_f32_bf16_e32 v64, v79, v79
	v_dot2c_f32_bf16_e32 v64, v80, v80
	s_waitcnt lgkmcnt(5)
	v_mfma_f32_16x16x32_bf16 v[172:175], v[176:179], v[78:81], v[172:175]
	v_dot2c_f32_bf16_e32 v64, v81, v81
	v_dot2c_f32_bf16_e32 v64, v74, v74
	v_dot2c_f32_bf16_e32 v64, v75, v75
	s_waitcnt lgkmcnt(4)
	v_mfma_f32_16x16x32_bf16 v[172:175], v[180:183], v[78:81], v[172:175]
	ds_read_b128 v[176:179], v133 offset:15360
	ds_read_b128 v[180:183], v133 offset:48128
	v_dot2c_f32_bf16_e32 v64, v76, v76
	v_dot2c_f32_bf16_e32 v64, v77, v77
	s_waitcnt lgkmcnt(5)
	v_mfma_f32_16x16x32_bf16 v[172:175], v[222:225], v[74:77], v[172:175]
	s_waitcnt vmcnt(16)
	v_dot2c_f32_bf16_e32 v64, v70, v70
	v_dot2c_f32_bf16_e32 v64, v71, v71
	v_dot2c_f32_bf16_e32 v64, v72, v72
	s_waitcnt lgkmcnt(4)
	v_mfma_f32_16x16x32_bf16 v[172:175], v[226:229], v[74:77], v[172:175]
	ds_read_b128 v[222:225], v133 offset:16384
	ds_read_b128 v[226:229], v133 offset:49152
	v_dot2c_f32_bf16_e32 v64, v73, v73
	v_dot2c_f32_bf16_e32 v64, v66, v66
	s_waitcnt lgkmcnt(5)
	v_mfma_f32_16x16x32_bf16 v[172:175], v[230:233], v[70:73], v[172:175]
	v_dot2c_f32_bf16_e32 v64, v67, v67
	v_dot2c_f32_bf16_e32 v64, v68, v68
	v_dot2c_f32_bf16_e32 v64, v69, v69
	s_waitcnt lgkmcnt(4)
	v_mfma_f32_16x16x32_bf16 v[172:175], v[234:237], v[70:73], v[172:175]
	ds_read_b128 v[230:233], v133 offset:17408
	ds_read_b128 v[234:237], v133 offset:50176
	s_waitcnt lgkmcnt(5)
	v_mfma_f32_16x16x32_bf16 v[172:175], v[176:179], v[66:69], v[172:175]
	s_waitcnt lgkmcnt(4)
	v_mfma_f32_16x16x32_bf16 v[172:175], v[180:183], v[66:69], v[172:175]
	ds_read_b128 v[176:179], v133 offset:18432
	ds_read_b128 v[180:183], v133 offset:51200
	s_waitcnt vmcnt(14)
	v_dot2c_f32_bf16_e32 v64, v60, v60
	v_dot2c_f32_bf16_e32 v64, v61, v61
	v_dot2c_f32_bf16_e32 v64, v62, v62
	s_waitcnt lgkmcnt(5)
	v_mfma_f32_16x16x32_bf16 v[172:175], v[222:225], v[60:63], v[172:175]
	v_dot2c_f32_bf16_e32 v64, v63, v63
	v_dot2c_f32_bf16_e32 v64, v56, v56
	v_dot2c_f32_bf16_e32 v64, v57, v57
	s_waitcnt lgkmcnt(4)
	v_mfma_f32_16x16x32_bf16 v[172:175], v[226:229], v[60:63], v[172:175]
	ds_read_b128 v[222:225], v133 offset:19456
	ds_read_b128 v[226:229], v133 offset:52224
	v_dot2c_f32_bf16_e32 v64, v58, v58
	v_dot2c_f32_bf16_e32 v64, v59, v59
	s_waitcnt lgkmcnt(5)
	v_mfma_f32_16x16x32_bf16 v[172:175], v[230:233], v[56:59], v[172:175]
	s_waitcnt vmcnt(12)
	v_dot2c_f32_bf16_e32 v64, v52, v52
	v_dot2c_f32_bf16_e32 v64, v53, v53
	v_dot2c_f32_bf16_e32 v64, v54, v54
	s_waitcnt lgkmcnt(4)
	v_mfma_f32_16x16x32_bf16 v[172:175], v[234:237], v[56:59], v[172:175]
	ds_read_b128 v[230:233], v133 offset:20480
	ds_read_b128 v[234:237], v133 offset:53248
	v_dot2c_f32_bf16_e32 v64, v55, v55
	v_dot2c_f32_bf16_e32 v64, v48, v48
	s_waitcnt lgkmcnt(5)
	v_mfma_f32_16x16x32_bf16 v[172:175], v[176:179], v[52:55], v[172:175]
	v_dot2c_f32_bf16_e32 v64, v49, v49
	v_dot2c_f32_bf16_e32 v64, v50, v50
	v_dot2c_f32_bf16_e32 v64, v51, v51
	s_waitcnt lgkmcnt(4)
	v_mfma_f32_16x16x32_bf16 v[172:175], v[180:183], v[52:55], v[172:175]
	ds_read_b128 v[176:179], v133 offset:21504
	ds_read_b128 v[180:183], v133 offset:54272
	s_waitcnt lgkmcnt(5)
	v_mfma_f32_16x16x32_bf16 v[172:175], v[222:225], v[48:51], v[172:175]
	s_waitcnt lgkmcnt(4)
	v_mfma_f32_16x16x32_bf16 v[172:175], v[226:229], v[48:51], v[172:175]
	ds_read_b128 v[222:225], v133 offset:22528
	ds_read_b128 v[226:229], v133 offset:55296
	s_waitcnt vmcnt(10)
	v_dot2c_f32_bf16_e32 v64, v44, v44
	v_dot2c_f32_bf16_e32 v64, v45, v45
	v_dot2c_f32_bf16_e32 v64, v46, v46
	s_waitcnt lgkmcnt(5)
	v_mfma_f32_16x16x32_bf16 v[172:175], v[230:233], v[44:47], v[172:175]
	v_dot2c_f32_bf16_e32 v64, v47, v47
	v_dot2c_f32_bf16_e32 v64, v40, v40
	v_dot2c_f32_bf16_e32 v64, v41, v41
	s_waitcnt lgkmcnt(4)
	v_mfma_f32_16x16x32_bf16 v[172:175], v[234:237], v[44:47], v[172:175]
	ds_read_b128 v[230:233], v133 offset:23552
	ds_read_b128 v[234:237], v133 offset:56320
	v_dot2c_f32_bf16_e32 v64, v42, v42
	v_dot2c_f32_bf16_e32 v64, v43, v43
	s_waitcnt lgkmcnt(5)
	v_mfma_f32_16x16x32_bf16 v[172:175], v[176:179], v[40:43], v[172:175]
	s_waitcnt vmcnt(8)
	v_dot2c_f32_bf16_e32 v64, v36, v36
	v_dot2c_f32_bf16_e32 v64, v37, v37
	v_dot2c_f32_bf16_e32 v64, v38, v38
	s_waitcnt lgkmcnt(4)
	v_mfma_f32_16x16x32_bf16 v[172:175], v[180:183], v[40:43], v[172:175]
	ds_read_b128 v[176:179], v133 offset:24576
	ds_read_b128 v[180:183], v133 offset:57344
	v_dot2c_f32_bf16_e32 v64, v39, v39
	v_dot2c_f32_bf16_e32 v64, v32, v32
	s_waitcnt lgkmcnt(5)
	v_mfma_f32_16x16x32_bf16 v[172:175], v[222:225], v[36:39], v[172:175]
	v_dot2c_f32_bf16_e32 v64, v33, v33
	v_dot2c_f32_bf16_e32 v64, v34, v34
	v_dot2c_f32_bf16_e32 v64, v35, v35
	s_waitcnt lgkmcnt(4)
	v_mfma_f32_16x16x32_bf16 v[172:175], v[226:229], v[36:39], v[172:175]
	ds_read_b128 v[222:225], v133 offset:25600
	ds_read_b128 v[226:229], v133 offset:58368
	s_waitcnt lgkmcnt(5)
	v_mfma_f32_16x16x32_bf16 v[172:175], v[230:233], v[32:35], v[172:175]
	s_waitcnt lgkmcnt(4)
	v_mfma_f32_16x16x32_bf16 v[172:175], v[234:237], v[32:35], v[172:175]
	ds_read_b128 v[230:233], v133 offset:26624
	ds_read_b128 v[234:237], v133 offset:59392
	s_waitcnt vmcnt(6)
	v_dot2c_f32_bf16_e32 v64, v28, v28
	v_dot2c_f32_bf16_e32 v64, v29, v29
	v_dot2c_f32_bf16_e32 v64, v30, v30
	s_waitcnt lgkmcnt(5)
	v_mfma_f32_16x16x32_bf16 v[172:175], v[176:179], v[28:31], v[172:175]
	v_dot2c_f32_bf16_e32 v64, v31, v31
	v_dot2c_f32_bf16_e32 v64, v24, v24
	v_dot2c_f32_bf16_e32 v64, v25, v25
	s_waitcnt lgkmcnt(4)
	v_mfma_f32_16x16x32_bf16 v[172:175], v[180:183], v[28:31], v[172:175]
	ds_read_b128 v[176:179], v133 offset:27648
	ds_read_b128 v[180:183], v133 offset:60416
	v_dot2c_f32_bf16_e32 v64, v26, v26
	v_dot2c_f32_bf16_e32 v64, v27, v27
	s_waitcnt lgkmcnt(5)
	v_mfma_f32_16x16x32_bf16 v[172:175], v[222:225], v[24:27], v[172:175]
	s_waitcnt vmcnt(4)
	v_dot2c_f32_bf16_e32 v64, v20, v20
	v_dot2c_f32_bf16_e32 v64, v21, v21
	v_dot2c_f32_bf16_e32 v64, v22, v22
	s_waitcnt lgkmcnt(4)
	v_mfma_f32_16x16x32_bf16 v[172:175], v[226:229], v[24:27], v[172:175]
	ds_read_b128 v[222:225], v133 offset:28672
	ds_read_b128 v[226:229], v133 offset:61440
	v_dot2c_f32_bf16_e32 v64, v23, v23
	v_dot2c_f32_bf16_e32 v64, v16, v16
	s_waitcnt lgkmcnt(5)
	v_mfma_f32_16x16x32_bf16 v[172:175], v[230:233], v[20:23], v[172:175]
	v_dot2c_f32_bf16_e32 v64, v17, v17
	v_dot2c_f32_bf16_e32 v64, v18, v18
	v_dot2c_f32_bf16_e32 v64, v19, v19
	s_waitcnt lgkmcnt(4)
	v_mfma_f32_16x16x32_bf16 v[172:175], v[234:237], v[20:23], v[172:175]
	ds_read_b128 v[230:233], v133 offset:29696
	ds_read_b128 v[234:237], v133 offset:62464
	s_waitcnt lgkmcnt(5)
	v_mfma_f32_16x16x32_bf16 v[172:175], v[176:179], v[16:19], v[172:175]
	s_waitcnt lgkmcnt(4)
	v_mfma_f32_16x16x32_bf16 v[172:175], v[180:183], v[16:19], v[172:175]
	ds_read_b128 v[176:179], v133 offset:30720
	ds_read_b128 v[180:183], v133 offset:63488
	s_waitcnt vmcnt(2)
	v_dot2c_f32_bf16_e32 v64, v12, v12
	v_dot2c_f32_bf16_e32 v64, v13, v13
	v_dot2c_f32_bf16_e32 v64, v14, v14
	s_waitcnt lgkmcnt(5)
	v_mfma_f32_16x16x32_bf16 v[172:175], v[222:225], v[12:15], v[172:175]
	v_dot2c_f32_bf16_e32 v64, v15, v15
	v_dot2c_f32_bf16_e32 v64, v8, v8
	v_dot2c_f32_bf16_e32 v64, v9, v9
	s_waitcnt lgkmcnt(4)
	v_mfma_f32_16x16x32_bf16 v[172:175], v[226:229], v[12:15], v[172:175]
	ds_read_b128 v[222:225], v133 offset:31744
	ds_read_b128 v[226:229], v133 offset:64512
	v_dot2c_f32_bf16_e32 v64, v10, v10
	v_dot2c_f32_bf16_e32 v64, v11, v11
	s_waitcnt lgkmcnt(5)
	v_mfma_f32_16x16x32_bf16 v[172:175], v[230:233], v[8:11], v[172:175]
	s_waitcnt vmcnt(0)
	v_dot2c_f32_bf16_e32 v64, v4, v4
	v_dot2c_f32_bf16_e32 v64, v5, v5
	v_dot2c_f32_bf16_e32 v64, v6, v6
	s_waitcnt lgkmcnt(4)
	v_mfma_f32_16x16x32_bf16 v[172:175], v[234:237], v[8:11], v[172:175]
	v_dot2c_f32_bf16_e32 v64, v7, v7
	v_dot2c_f32_bf16_e32 v64, v0, v0
	s_waitcnt lgkmcnt(3)
	v_mfma_f32_16x16x32_bf16 v[172:175], v[176:179], v[4:7], v[172:175]
	v_dot2c_f32_bf16_e32 v64, v1, v1
	v_dot2c_f32_bf16_e32 v64, v2, v2
	v_dot2c_f32_bf16_e32 v64, v3, v3
	s_waitcnt lgkmcnt(2)
	v_mfma_f32_16x16x32_bf16 v[172:175], v[180:183], v[4:7], v[172:175]
	s_waitcnt lgkmcnt(1)
	v_mfma_f32_16x16x32_bf16 v[172:175], v[222:225], v[0:3], v[172:175]
	s_waitcnt lgkmcnt(0)
	v_mfma_f32_16x16x32_bf16 v[172:175], v[226:229], v[0:3], v[172:175]
	ds_bpermute_b32 v142, v148, v64
	v_add_u32_e32 v171, s25, v132
	ds_read_b128 v[176:179], v171
	s_mov_b32 s14, 0xc2ce8ed0
	s_mov_b32 s15, 0x42b17218
	s_waitcnt lgkmcnt(1)
	v_add_f32_e32 v64, v64, v142
	ds_bpermute_b32 v142, v149, v64
	s_waitcnt lgkmcnt(1)
	v_pk_add_f32 v[146:147], v[176:177], 0 op_sel_hi:[1,0]
	s_waitcnt lgkmcnt(0)
	v_add_f32_e32 v64, v64, v142
	v_pk_add_f32 v[142:143], v[178:179], 0 op_sel_hi:[1,0]
	ds_read_b128 v[176:179], v171 offset:64
	v_fmamk_f32 v64, v64, 0x3a800000, v200
	s_waitcnt lgkmcnt(0)
	v_pk_add_f32 v[142:143], v[142:143], v[178:179]
	v_pk_add_f32 v[146:147], v[146:147], v[176:177]
	ds_read_b128 v[176:179], v171 offset:128
	s_waitcnt lgkmcnt(0)
	v_pk_add_f32 v[142:143], v[142:143], v[178:179]
	v_pk_add_f32 v[146:147], v[146:147], v[176:177]
	ds_read_b128 v[176:179], v171 offset:192
	s_waitcnt lgkmcnt(0)
	v_pk_add_f32 v[142:143], v[142:143], v[178:179]
	v_pk_add_f32 v[146:147], v[146:147], v[176:177]
	ds_read_b128 v[176:179], v171 offset:256
	s_waitcnt lgkmcnt(0)
	v_pk_add_f32 v[142:143], v[142:143], v[178:179]
	v_pk_add_f32 v[146:147], v[146:147], v[176:177]
	ds_read_b128 v[176:179], v171 offset:320
	s_waitcnt lgkmcnt(0)
	v_pk_add_f32 v[142:143], v[142:143], v[178:179]
	v_pk_add_f32 v[146:147], v[146:147], v[176:177]
	ds_read_b128 v[176:179], v171 offset:384
	s_waitcnt lgkmcnt(0)
	v_pk_add_f32 v[142:143], v[142:143], v[178:179]
	v_pk_add_f32 v[146:147], v[146:147], v[176:177]
	ds_read_b128 v[176:179], v171 offset:448
	s_waitcnt lgkmcnt(0)
	v_pk_add_f32 v[178:179], v[142:143], v[178:179]
	v_rsq_f32_e32 v142, v64
	v_pk_add_f32 v[146:147], v[146:147], v[176:177]
	v_pk_fma_f32 v[174:175], v[174:175], v[142:143], v[178:179] op_sel_hi:[1,0,1]
	v_pk_fma_f32 v[146:147], v[172:173], v[142:143], v[146:147] op_sel_hi:[1,0,1]
	v_max_f32_e32 v64, v174, v175
	v_max3_f32 v64, v146, v147, v64
	ds_bpermute_b32 v143, v148, v64
	s_waitcnt lgkmcnt(0)
	v_max_f32_e32 v143, v143, v143
	v_max_f32_e32 v64, v64, v143
	ds_bpermute_b32 v143, v149, v64
	s_waitcnt lgkmcnt(0)
	v_max_f32_e32 v143, v143, v143
	v_max_f32_e32 v64, v64, v143
	v_sub_f32_e32 v143, v146, v64
	v_mul_f32_e32 v146, 0x3fb8aa3b, v143
	v_fma_f32 v171, v143, s94, -v146
	v_rndne_f32_e32 v172, v146
	v_fmac_f32_e32 v171, 0x32a5705f, v143
	v_sub_f32_e32 v146, v146, v172
	v_add_f32_e32 v146, v146, v171
	v_exp_f32_e32 v146, v146
	v_cvt_i32_f32_e32 v171, v172
	v_cmp_ngt_f32_e32 vcc, s14, v143
	v_ldexp_f32 v146, v146, v171
	s_nop 0
	v_cndmask_b32_e32 v146, 0, v146, vcc
	v_cmp_nlt_f32_e32 vcc, s15, v143
	v_sub_f32_e32 v143, v147, v64
	s_nop 0
	v_cndmask_b32_e32 v172, v204, v146, vcc
	v_mul_f32_e32 v146, 0x3fb8aa3b, v143
	v_fma_f32 v147, v143, s94, -v146
	v_rndne_f32_e32 v171, v146
	v_fmac_f32_e32 v147, 0x32a5705f, v143
	v_sub_f32_e32 v146, v146, v171
	v_add_f32_e32 v146, v146, v147
	v_exp_f32_e32 v146, v146
	v_cvt_i32_f32_e32 v147, v171
	v_cmp_ngt_f32_e32 vcc, s14, v143
	v_ldexp_f32 v146, v146, v147
	s_nop 0
	v_cndmask_b32_e32 v146, 0, v146, vcc
	v_cmp_nlt_f32_e32 vcc, s15, v143
	v_sub_f32_e32 v143, v174, v64
	v_sub_f32_e32 v64, v175, v64
	v_cndmask_b32_e32 v171, v204, v146, vcc
	v_mul_f32_e32 v146, 0x3fb8aa3b, v143
	v_fma_f32 v147, v143, s94, -v146
	v_rndne_f32_e32 v173, v146
	v_fmac_f32_e32 v147, 0x32a5705f, v143
	v_sub_f32_e32 v146, v146, v173
	v_add_f32_e32 v146, v146, v147
	v_exp_f32_e32 v146, v146
	v_cvt_i32_f32_e32 v147, v173
	v_cmp_ngt_f32_e32 vcc, s14, v143
	v_ldexp_f32 v146, v146, v147
	s_nop 0
	v_cndmask_b32_e32 v146, 0, v146, vcc
	v_cmp_nlt_f32_e32 vcc, s15, v143
	v_mul_f32_e32 v143, 0x3fb8aa3b, v64
	v_rndne_f32_e32 v147, v143
	v_cndmask_b32_e32 v173, v204, v146, vcc
	v_fma_f32 v146, v64, s94, -v143
	v_fmac_f32_e32 v146, 0x32a5705f, v64
	v_sub_f32_e32 v143, v143, v147
	v_add_f32_e32 v143, v143, v146
	v_exp_f32_e32 v143, v143
	v_cvt_i32_f32_e32 v146, v147
	v_cmp_ngt_f32_e32 vcc, s14, v64
	v_ldexp_f32 v143, v143, v146
	s_nop 0
	v_cndmask_b32_e32 v143, 0, v143, vcc
	v_cmp_nlt_f32_e32 vcc, s15, v64
	v_add_f32_e32 v64, v172, v171
	s_mov_b64 s[14:15], -1
	v_cndmask_b32_e32 v174, v204, v143, vcc
	v_add_f32_e32 v143, v173, v174
	v_add_f32_e32 v64, v64, v143
	ds_bpermute_b32 v143, v148, v64
	s_and_b64 vcc, exec, s[12:13]
	s_waitcnt lgkmcnt(0)
	v_add_f32_e32 v64, v64, v143
	ds_bpermute_b32 v175, v149, v64
	s_cbranch_vccz .LBB0_987
	v_lshl_or_b32 v146, s29, 4, v152
	v_ashrrev_i32_e32 v147, 31, v146
	v_lshlrev_b64 v[146:147], 16, v[146:147]
	v_lshl_add_u64 v[146:147], s[0:1], 0, v[146:147]
	s_lshl_b32 s78, s11, 2
	v_lshl_add_u64 v[146:147], v[146:147], 0, s[78:79]
	s_mov_b64 s[12:13], 0x6fbffc00
	v_lshl_add_u64 v[146:147], v[146:147], 0, s[12:13]
	s_mov_b64 s[14:15], 0

	.amdhsa_kernel _Z8mega_fwd4Args
		.amdhsa_group_segment_fixed_size 0
		.amdhsa_private_segment_fixed_size 0
		.amdhsa_kernarg_size 416
		.amdhsa_user_sgpr_count 2
		.amdhsa_user_sgpr_dispatch_ptr 0
		.amdhsa_user_sgpr_queue_ptr 0
		.amdhsa_user_sgpr_kernarg_segment_ptr 1
		.amdhsa_user_sgpr_dispatch_id 0
		.amdhsa_user_sgpr_kernarg_preload_length 0
		.amdhsa_user_sgpr_kernarg_preload_offset 0
		.amdhsa_user_sgpr_private_segment_size 0
		.amdhsa_uses_dynamic_stack 0
		.amdhsa_enable_private_segment 0
		.amdhsa_system_sgpr_workgroup_id_x 1
		.amdhsa_system_sgpr_workgroup_id_y 0
		.amdhsa_system_sgpr_workgroup_id_z 0
		.amdhsa_system_sgpr_workgroup_info 0
		.amdhsa_system_vgpr_workitem_id 0
		.amdhsa_next_free_vgpr 256
		.amdhsa_next_free_sgpr 102
		.amdhsa_accum_offset 256
		.amdhsa_reserve_vcc 1
		.amdhsa_float_round_mode_32 0
		.amdhsa_float_round_mode_16_64 0
		.amdhsa_float_denorm_mode_32 3
		.amdhsa_float_denorm_mode_16_64 3
		.amdhsa_dx10_clamp 1
		.amdhsa_ieee_mode 1
		.amdhsa_fp16_overflow 0
		.amdhsa_tg_split 0
		.amdhsa_exception_fp_ieee_invalid_op 0
		.amdhsa_exception_fp_denorm_src 0
		.amdhsa_exception_fp_ieee_div_zero 0
		.amdhsa_exception_fp_ieee_overflow 0
		.amdhsa_exception_fp_ieee_underflow 0
		.amdhsa_exception_fp_ieee_inexact 0
		.amdhsa_exception_int_div_zero 0
	.end_amdhsa_kernel

amdhsa.kernels:
  - .agpr_count:     0
    .args:
      - .offset:         0
        .size:           160
        .value_kind:     by_value
      - .offset:         160
        .size:           4
        .value_kind:     hidden_block_count_x
      - .offset:         164
        .size:           4
        .value_kind:     hidden_block_count_y
      - .offset:         168
        .size:           4
        .value_kind:     hidden_block_count_z
      - .offset:         172
        .size:           2
        .value_kind:     hidden_group_size_x
      - .offset:         174
        .size:           2
        .value_kind:     hidden_group_size_y
      - .offset:         176
        .size:           2
        .value_kind:     hidden_group_size_z
      - .offset:         178
        .size:           2
        .value_kind:     hidden_remainder_x
      - .offset:         180
        .size:           2
        .value_kind:     hidden_remainder_y
      - .offset:         182
        .size:           2
        .value_kind:     hidden_remainder_z
      - .offset:         200
        .size:           8
        .value_kind:     hidden_global_offset_x
      - .offset:         208
        .size:           8
        .value_kind:     hidden_global_offset_y
      - .offset:         216
        .size:           8
        .value_kind:     hidden_global_offset_z
      - .offset:         224
        .size:           2
        .value_kind:     hidden_grid_dims
      - .offset:         280
        .size:           4
        .value_kind:     hidden_dynamic_lds_size
    .group_segment_fixed_size: 0
    .kernarg_segment_align: 8
    .kernarg_segment_size: 416
    .language:       OpenCL C
    .language_version:
      - 2
      - 0
    .max_flat_workgroup_size: 512
    .name:           _Z8mega_fwd4Args
    .private_segment_fixed_size: 0
    .sgpr_count:     108
    .sgpr_spill_count: 333
    .symbol:         _Z8mega_fwd4Args.kd
    .uniform_work_group_size: 1
    .uses_dynamic_stack: false
    .vgpr_count:     256
    .vgpr_spill_count: 0
    .wavefront_size: 64
